# norm1(layer 0) modulation tables in one batch; norm2 row-pair loop issues all 16 X pieces before waiting
# baseline (speedup 1.0000x reference)
.LBB0_272:
	s_lshl_b32 s4, s6, 12
	s_add_i32 s13, s6, 1
	s_add_i32 s24, s12, s4
	s_lshl_b32 s25, s13, 12
	v_readlane_b32 s28, v255, 19
	s_cmp_ge_i32 s24, s25
	v_readlane_b32 s29, v255, 20
	s_cbranch_scc1 .LBB0_271
	s_ashr_i32 s41, s40, 31
	s_lshl_b64 s[4:5], s[40:41], 11
	s_mul_i32 s20, s6, 0x3000
	v_lshl_add_u64 v[74:75], v[72:73], 0, s[4:5]
	s_lshl_b64 s[4:5], s[40:41], 13
	s_lshl_b64 s[6:7], s[20:21], 2
	s_add_u32 s6, s10, s6
	s_addc_u32 s7, s11, s7
	s_add_u32 s8, s6, 0x2000
	s_addc_u32 s9, s7, 0
	global_load_dwordx4 v[2:5], v[62:63], off
	global_load_dwordx4 v[76:79], v111, s[8:9]
	global_load_dwordx4 v[6:9], v[62:63], off offset:1024
	global_load_dwordx4 v[80:83], v114, s[8:9]
	global_load_dwordx4 v[10:13], v[62:63], off offset:2048
	global_load_dwordx4 v[84:87], v115, s[8:9]
	global_load_dwordx4 v[14:17], v[62:63], off offset:3072
	global_load_dwordx4 v[88:91], v116, s[8:9]
	global_load_dwordx4 v[18:21], v[64:65], off
	global_load_dwordx4 v[92:95], v117, s[8:9]
	global_load_dwordx4 v[22:25], v[66:67], off
	global_load_dwordx4 v[96:99], v118, s[8:9]
	global_load_dwordx4 v[26:29], v[68:69], off
	global_load_dwordx4 v[100:103], v119, s[8:9]
	global_load_dwordx4 v[30:33], v[70:71], off
	global_load_dwordx4 v[104:107], v120, s[8:9]
	s_waitcnt vmcnt(0)
	v_pk_add_f32 v[78:79], v[78:79], 1.0 op_sel_hi:[1,0]
	v_pk_add_f32 v[76:77], v[76:77], 1.0 op_sel_hi:[1,0]
	v_pk_mul_f32 v[34:35], v[4:5], v[78:79]
	v_pk_mul_f32 v[78:79], v[2:3], v[76:77]
	v_mov_b64_e32 v[76:77], v[34:35]
	v_pk_add_f32 v[82:83], v[82:83], 1.0 op_sel_hi:[1,0]
	v_pk_add_f32 v[80:81], v[80:81], 1.0 op_sel_hi:[1,0]
	v_pk_mul_f32 v[34:35], v[8:9], v[82:83]
	v_pk_mul_f32 v[82:83], v[6:7], v[80:81]
	v_mov_b64_e32 v[80:81], v[34:35]
	v_pk_add_f32 v[86:87], v[86:87], 1.0 op_sel_hi:[1,0]
	v_pk_add_f32 v[84:85], v[84:85], 1.0 op_sel_hi:[1,0]
	v_pk_mul_f32 v[34:35], v[12:13], v[86:87]
	v_pk_mul_f32 v[86:87], v[10:11], v[84:85]
	v_mov_b64_e32 v[84:85], v[34:35]
	v_pk_add_f32 v[90:91], v[90:91], 1.0 op_sel_hi:[1,0]
	v_pk_add_f32 v[88:89], v[88:89], 1.0 op_sel_hi:[1,0]
	v_pk_mul_f32 v[34:35], v[16:17], v[90:91]
	v_pk_mul_f32 v[90:91], v[14:15], v[88:89]
	v_mov_b64_e32 v[88:89], v[34:35]
	v_pk_add_f32 v[94:95], v[94:95], 1.0 op_sel_hi:[1,0]
	v_pk_add_f32 v[92:93], v[92:93], 1.0 op_sel_hi:[1,0]
	v_pk_mul_f32 v[34:35], v[20:21], v[94:95]
	v_pk_mul_f32 v[94:95], v[18:19], v[92:93]
	v_mov_b64_e32 v[92:93], v[34:35]
	v_pk_add_f32 v[98:99], v[98:99], 1.0 op_sel_hi:[1,0]
	v_pk_add_f32 v[96:97], v[96:97], 1.0 op_sel_hi:[1,0]
	v_pk_mul_f32 v[34:35], v[24:25], v[98:99]
	v_pk_mul_f32 v[98:99], v[22:23], v[96:97]
	v_mov_b64_e32 v[96:97], v[34:35]
	v_pk_add_f32 v[102:103], v[102:103], 1.0 op_sel_hi:[1,0]
	v_pk_add_f32 v[100:101], v[100:101], 1.0 op_sel_hi:[1,0]
	v_pk_mul_f32 v[34:35], v[28:29], v[102:103]
	v_pk_mul_f32 v[102:103], v[26:27], v[100:101]
	v_mov_b64_e32 v[100:101], v[34:35]
	v_pk_add_f32 v[106:107], v[106:107], 1.0 op_sel_hi:[1,0]
	v_pk_add_f32 v[104:105], v[104:105], 1.0 op_sel_hi:[1,0]
	v_pk_mul_f32 v[34:35], v[32:33], v[106:107]
	v_pk_mul_f32 v[106:107], v[30:31], v[104:105]
	v_mov_b64_e32 v[104:105], v[34:35]
	global_load_dwordx4 v[2:5], v111, s[6:7]
	global_load_dwordx4 v[6:9], v111, s[6:7] offset:1024
	global_load_dwordx4 v[10:13], v111, s[6:7] offset:2048
	global_load_dwordx4 v[14:17], v111, s[6:7] offset:3072
	global_load_dwordx4 v[18:21], v117, s[6:7]
	global_load_dwordx4 v[22:25], v118, s[6:7]
	global_load_dwordx4 v[26:29], v119, s[6:7]
	global_load_dwordx4 v[30:33], v120, s[6:7]
	v_and_b32_e32 v34, 64, v226
	v_add_u32_e32 v34, 64, v34
	v_xor_b32_e32 v35, 1, v226
	v_cmp_lt_i32_e32 vcc, v35, v34
	s_load_dwordx2 s[6:7], s[44:45], 0x0
	s_nop 0
	v_cndmask_b32_e32 v35, v226, v35, vcc
	v_lshlrev_b32_e32 v121, 2, v35
	v_xor_b32_e32 v35, 2, v226
	v_cmp_lt_i32_e32 vcc, v35, v34
	s_nop 1
	v_cndmask_b32_e32 v35, v226, v35, vcc
	v_lshlrev_b32_e32 v122, 2, v35
	v_xor_b32_e32 v35, 4, v226
	v_cmp_lt_i32_e32 vcc, v35, v34
	s_nop 1
	v_cndmask_b32_e32 v35, v226, v35, vcc
	v_lshlrev_b32_e32 v123, 2, v35
	v_xor_b32_e32 v35, 8, v226
	v_cmp_lt_i32_e32 vcc, v35, v34
	s_nop 1
	v_cndmask_b32_e32 v34, v226, v35, vcc
	v_lshlrev_b32_e32 v124, 2, v34
	s_waitcnt lgkmcnt(0)
	v_lshl_add_u64 v[34:35], s[6:7], 0, v[0:1]
	v_lshl_add_u64 v[34:35], v[34:35], 0, s[4:5]
	s_mov_b64 s[4:5], 0x1c00
	v_lshl_add_u64 v[108:109], v[34:35], 0, s[4:5]

.LBB0_1300:
	v_lshl_add_u64 v[2:3], s[58:59], 0, v[60:61]
	v_add_co_u32_e32 v4, vcc, 0x11100000, v2
	v_lshl_add_u64 v[158:159], s[58:59], 0, v[58:59]
	s_nop 0
	v_addc_co_u32_e32 v5, vcc, 0, v3, vcc
	global_load_dwordx2 v[94:95], v[4:5], off nt
	v_add_co_u32_e32 v96, vcc, 0x11101000, v2
	s_nop 1
	v_addc_co_u32_e32 v97, vcc, 0, v3, vcc
	global_load_dwordx2 v[98:99], v[96:97], off nt
	global_load_dwordx2 v[100:101], v[4:5], off offset:512 nt
	global_load_dwordx2 v[106:107], v[96:97], off offset:512 nt
	global_load_dwordx2 v[108:109], v[4:5], off offset:1024 nt
	global_load_dwordx2 v[110:111], v[96:97], off offset:1024 nt
	global_load_dwordx2 v[20:21], v[4:5], off offset:1536 nt
	global_load_dwordx2 v[18:19], v[96:97], off offset:1536 nt
	global_load_dwordx2 v[16:17], v[4:5], off offset:2048 nt
	global_load_dwordx2 v[14:15], v[96:97], off offset:2048 nt
	global_load_dwordx2 v[12:13], v[4:5], off offset:2560 nt
	global_load_dwordx2 v[10:11], v[96:97], off offset:2560 nt
	global_load_dwordx2 v[8:9], v[4:5], off offset:3072 nt
	global_load_dwordx2 v[6:7], v[96:97], off offset:3072 nt
	global_load_dwordx2 v[2:3], v[4:5], off offset:3584 nt
	s_nop 0
	global_load_dwordx2 v[4:5], v[96:97], off offset:3584 nt
	s_waitcnt vmcnt(15)
	v_and_b32_e32 v157, 0xffff0000, v94
	v_and_b32_e32 v155, 0xffff0000, v95
	v_lshlrev_b32_e32 v156, 16, v94
	v_lshlrev_b32_e32 v154, 16, v95
	v_mul_f32_e32 v47, v157, v157
	v_mul_f32_e32 v49, v155, v155
	v_fmac_f32_e32 v47, v156, v156
	v_fmac_f32_e32 v49, v154, v154
	v_add_f32_e32 v47, v47, v49
	s_waitcnt vmcnt(14)
	v_and_b32_e32 v153, 0xffff0000, v98
	v_and_b32_e32 v119, 0xffff0000, v99
	v_lshlrev_b32_e32 v152, 16, v98
	v_lshlrev_b32_e32 v118, 16, v99
	v_mul_f32_e32 v49, v153, v153
	v_mul_f32_e32 v51, v119, v119
	v_fmac_f32_e32 v49, v152, v152
	v_fmac_f32_e32 v51, v118, v118
	s_waitcnt vmcnt(13)
	v_and_b32_e32 v151, 0xffff0000, v100
	v_and_b32_e32 v149, 0xffff0000, v101
	v_add_f32_e32 v49, v49, v51
	v_lshlrev_b32_e32 v150, 16, v100
	v_lshlrev_b32_e32 v148, 16, v101
	v_mul_f32_e32 v51, v151, v151
	v_mul_f32_e32 v53, v149, v149
	v_fmac_f32_e32 v51, v150, v150
	v_fmac_f32_e32 v53, v148, v148
	s_waitcnt vmcnt(12)
	v_and_b32_e32 v147, 0xffff0000, v106
	v_and_b32_e32 v145, 0xffff0000, v107
	v_add_f32_e32 v51, v51, v53
	v_lshlrev_b32_e32 v146, 16, v106
	v_lshlrev_b32_e32 v144, 16, v107
	v_add_f32_e32 v47, v47, v51
	v_mul_f32_e32 v51, v147, v147
	v_mul_f32_e32 v53, v145, v145
	v_fmac_f32_e32 v51, v146, v146
	v_fmac_f32_e32 v53, v144, v144
	v_add_f32_e32 v51, v51, v53
	s_waitcnt vmcnt(11)
	v_and_b32_e32 v143, 0xffff0000, v108
	v_and_b32_e32 v141, 0xffff0000, v109
	v_add_f32_e32 v49, v49, v51
	v_lshlrev_b32_e32 v142, 16, v108
	v_lshlrev_b32_e32 v140, 16, v109
	v_mul_f32_e32 v51, v143, v143
	v_mul_f32_e32 v53, v141, v141
	v_fmac_f32_e32 v51, v142, v142
	v_fmac_f32_e32 v53, v140, v140
	s_waitcnt vmcnt(9)
	v_and_b32_e32 v131, 0xffff0000, v20
	v_and_b32_e32 v129, 0xffff0000, v21
	v_and_b32_e32 v139, 0xffff0000, v110
	v_and_b32_e32 v137, 0xffff0000, v111
	v_add_f32_e32 v51, v51, v53
	v_lshlrev_b32_e32 v130, 16, v20
	v_lshlrev_b32_e32 v128, 16, v21
	s_waitcnt vmcnt(8)
	v_lshlrev_b32_e32 v132, 16, v18
	v_and_b32_e32 v133, 0xffff0000, v18
	v_lshlrev_b32_e32 v134, 16, v19
	v_and_b32_e32 v135, 0xffff0000, v19
	v_mul_f32_e32 v18, v131, v131
	v_mul_f32_e32 v19, v129, v129
	s_waitcnt vmcnt(7)
	v_and_b32_e32 v127, 0xffff0000, v16
	v_and_b32_e32 v125, 0xffff0000, v17
	v_lshlrev_b32_e32 v138, 16, v110
	v_lshlrev_b32_e32 v136, 16, v111
	v_add_f32_e32 v47, v47, v51
	v_mul_f32_e32 v51, v139, v139
	v_mul_f32_e32 v53, v137, v137
	v_fmac_f32_e32 v18, v130, v130
	v_fmac_f32_e32 v19, v128, v128
	v_lshlrev_b32_e32 v126, 16, v16
	v_lshlrev_b32_e32 v124, 16, v17
	s_waitcnt vmcnt(6)
	v_lshlrev_b32_e32 v122, 16, v14
	v_and_b32_e32 v123, 0xffff0000, v14
	v_lshlrev_b32_e32 v120, 16, v15
	v_and_b32_e32 v121, 0xffff0000, v15
	v_mul_f32_e32 v14, v127, v127
	v_mul_f32_e32 v15, v125, v125
	v_fmac_f32_e32 v51, v138, v138
	v_fmac_f32_e32 v53, v136, v136
	v_add_f32_e32 v18, v18, v19
	v_mul_f32_e32 v19, v133, v133
	v_mul_f32_e32 v20, v135, v135
	v_fmac_f32_e32 v14, v126, v126
	v_fmac_f32_e32 v15, v124, v124
	v_add_f32_e32 v51, v51, v53
	v_fmac_f32_e32 v19, v132, v132
	v_fmac_f32_e32 v20, v134, v134
	v_add_f32_e32 v14, v14, v15
	v_mul_f32_e32 v15, v123, v123
	v_mul_f32_e32 v16, v121, v121
	v_add_f32_e32 v49, v49, v51
	v_add_f32_e32 v19, v19, v20
	v_fmac_f32_e32 v15, v122, v122
	v_fmac_f32_e32 v16, v120, v120
	s_waitcnt vmcnt(5)
	v_and_b32_e32 v117, 0xffff0000, v12
	v_and_b32_e32 v115, 0xffff0000, v13
	v_add_f32_e32 v18, v47, v18
	v_add_f32_e32 v19, v49, v19
	v_add_f32_e32 v15, v15, v16
	v_lshlrev_b32_e32 v116, 16, v12
	v_lshlrev_b32_e32 v114, 16, v13
	s_waitcnt vmcnt(4)
	v_lshlrev_b32_e32 v112, 16, v10
	v_and_b32_e32 v113, 0xffff0000, v10
	v_lshlrev_b32_e32 v110, 16, v11
	v_and_b32_e32 v111, 0xffff0000, v11
	v_mul_f32_e32 v10, v117, v117
	v_mul_f32_e32 v11, v115, v115
	s_waitcnt vmcnt(3)
	v_and_b32_e32 v109, 0xffff0000, v8
	v_and_b32_e32 v107, 0xffff0000, v9
	v_add_f32_e32 v14, v18, v14
	v_add_f32_e32 v15, v19, v15
	v_fmac_f32_e32 v10, v116, v116
	v_fmac_f32_e32 v11, v114, v114
	v_lshlrev_b32_e32 v108, 16, v8
	v_lshlrev_b32_e32 v106, 16, v9
	s_waitcnt vmcnt(2)
	v_lshlrev_b32_e32 v20, 16, v6
	v_and_b32_e32 v21, 0xffff0000, v6
	v_lshlrev_b32_e32 v18, 16, v7
	v_and_b32_e32 v19, 0xffff0000, v7
	v_mul_f32_e32 v6, v109, v109
	v_mul_f32_e32 v7, v107, v107
	s_waitcnt vmcnt(1)
	v_and_b32_e32 v101, 0xffff0000, v2
	v_and_b32_e32 v99, 0xffff0000, v3
	v_add_f32_e32 v10, v10, v11
	v_fmac_f32_e32 v6, v108, v108
	v_fmac_f32_e32 v7, v106, v106
	v_lshlrev_b32_e32 v100, 16, v2
	v_lshlrev_b32_e32 v98, 16, v3
	v_mul_f32_e32 v2, v101, v101
	v_mul_f32_e32 v3, v99, v99
	v_add_f32_e32 v10, v14, v10
	v_add_f32_e32 v6, v6, v7
	s_waitcnt vmcnt(0)
	v_and_b32_e32 v97, 0xffff0000, v4
	v_and_b32_e32 v95, 0xffff0000, v5
	v_fmac_f32_e32 v2, v100, v100
	v_fmac_f32_e32 v3, v98, v98
	v_add_f32_e32 v6, v10, v6
	v_lshlrev_b32_e32 v96, 16, v4
	v_lshlrev_b32_e32 v94, 16, v5
	v_add_f32_e32 v2, v2, v3
	v_mul_f32_e32 v3, v97, v97
	v_mul_f32_e32 v4, v95, v95
	v_add_f32_e32 v2, v6, v2
	v_fmac_f32_e32 v3, v96, v96
	v_fmac_f32_e32 v4, v94, v94
	v_add_f32_e32 v3, v3, v4
	ds_bpermute_b32 v4, v23, v2
	v_mul_f32_e32 v11, v113, v113
	v_mul_f32_e32 v12, v111, v111
	v_fmac_f32_e32 v11, v112, v112
	v_fmac_f32_e32 v12, v110, v110
	s_waitcnt lgkmcnt(0)
	v_add_f32_e32 v2, v2, v4
	ds_bpermute_b32 v4, v25, v2
	v_mul_f32_e32 v7, v21, v21
	v_mul_f32_e32 v8, v19, v19
	v_add_f32_e32 v11, v11, v12
	v_fmac_f32_e32 v7, v20, v20
	s_waitcnt lgkmcnt(0)
	v_add_f32_e32 v2, v2, v4
	ds_bpermute_b32 v4, v43, v2
	v_fmac_f32_e32 v8, v18, v18
	v_add_f32_e32 v11, v15, v11
	v_add_f32_e32 v7, v7, v8
	v_add_f32_e32 v7, v11, v7
	s_waitcnt lgkmcnt(0)
	v_add_f32_e32 v2, v2, v4
	ds_bpermute_b32 v4, v103, v2
	v_add_f32_e32 v3, v7, v3
	v_mov_b32_e32 v51, 0
	s_waitcnt lgkmcnt(0)
	v_add_f32_e32 v2, v2, v4
	v_mov_b32_e32 v4, v2
	s_nop 1
	v_permlane16_swap_b32_e32 v2, v4
	v_add_f32_e32 v2, v2, v4
	v_mov_b32_e32 v4, v2
	s_nop 1
	v_permlane32_swap_b32_e32 v2, v4
	v_add_f32_e32 v2, v2, v4
	v_fmamk_f32 v2, v2, 0x3a000000, v228
	v_cmp_gt_f32_e32 vcc, s82, v2
	v_mul_f32_e32 v4, 0x4f800000, v2
	s_nop 0
	v_cndmask_b32_e32 v2, v2, v4, vcc
	v_sqrt_f32_e32 v4, v2
	s_nop 0
	v_add_u32_e32 v5, -1, v4
	v_fma_f32 v6, -v5, v4, v2
	v_cmp_ge_f32_e64 s[44:45], 0, v6
	v_add_u32_e32 v6, 1, v4
	s_nop 0
	v_cndmask_b32_e64 v5, v4, v5, s[44:45]
	v_fma_f32 v4, -v6, v4, v2
	v_cmp_lt_f32_e64 s[44:45], 0, v4
	s_nop 1
	v_cndmask_b32_e64 v4, v5, v6, s[44:45]
	v_mul_f32_e32 v5, 0x37800000, v4
	v_cndmask_b32_e32 v4, v4, v5, vcc
	v_cmp_class_f32_e32 vcc, v2, v229
	s_nop 1
	v_cndmask_b32_e32 v2, v4, v2, vcc
	ds_bpermute_b32 v4, v23, v3
	s_waitcnt lgkmcnt(0)
	v_add_f32_e32 v3, v3, v4
	ds_bpermute_b32 v4, v25, v3
	s_waitcnt lgkmcnt(0)
	v_add_f32_e32 v3, v3, v4
	ds_bpermute_b32 v4, v43, v3
	s_waitcnt lgkmcnt(0)
	v_add_f32_e32 v3, v3, v4
	ds_bpermute_b32 v4, v103, v3
	s_waitcnt lgkmcnt(0)
	v_add_f32_e32 v3, v3, v4
	v_mov_b32_e32 v4, v3
	s_nop 1
	v_permlane16_swap_b32_e32 v3, v4
	v_add_f32_e32 v3, v3, v4
	v_mov_b32_e32 v4, v3
	s_nop 1
	v_permlane32_swap_b32_e32 v3, v4
	v_add_f32_e32 v3, v3, v4
	v_fmamk_f32 v3, v3, 0x3a000000, v228
	v_cmp_gt_f32_e32 vcc, s82, v3
	v_mul_f32_e32 v4, 0x4f800000, v3
	s_nop 0
	v_cndmask_b32_e32 v3, v3, v4, vcc
	v_sqrt_f32_e32 v4, v3
	s_nop 0
	v_add_u32_e32 v5, -1, v4
	v_fma_f32 v6, -v5, v4, v3
	v_cmp_ge_f32_e64 s[44:45], 0, v6
	v_add_u32_e32 v6, 1, v4
	s_nop 0
	v_cndmask_b32_e64 v5, v4, v5, s[44:45]
	v_fma_f32 v4, -v6, v4, v3
	v_cmp_lt_f32_e64 s[44:45], 0, v4
	s_nop 1
	v_cndmask_b32_e64 v4, v5, v6, s[44:45]
	v_mul_f32_e32 v5, 0x37800000, v4
	v_cndmask_b32_e32 v4, v4, v5, vcc
	v_cmp_class_f32_e32 vcc, v3, v229
	s_nop 1
	v_cndmask_b32_e32 v3, v4, v3, vcc
	v_div_scale_f32 v4, s[4:5], v2, v2, 1.0
	v_rcp_f32_e32 v5, v4
	s_nop 0
	v_fma_f32 v6, -v4, v5, 1.0
	v_fmac_f32_e32 v5, v6, v5
	v_div_scale_f32 v6, vcc, 1.0, v2, 1.0
	v_mul_f32_e32 v7, v6, v5
	v_fma_f32 v8, -v4, v7, v6
	v_fmac_f32_e32 v7, v8, v5
	v_fma_f32 v4, -v4, v7, v6
	v_div_fmas_f32 v4, v4, v5, v7
	v_div_fixup_f32 v102, v4, v2, 1.0
	v_div_scale_f32 v2, s[4:5], v3, v3, 1.0
	v_rcp_f32_e32 v4, v2
	v_pk_mul_f32 v[156:157], v[102:103], v[156:157] op_sel_hi:[0,1]
	v_pk_mul_f32 v[154:155], v[102:103], v[154:155] op_sel_hi:[0,1]
	v_fma_f32 v5, -v2, v4, 1.0
	v_fmac_f32_e32 v4, v5, v4
	v_div_scale_f32 v5, vcc, 1.0, v3, 1.0
	v_mul_f32_e32 v6, v5, v4
	v_fma_f32 v7, -v2, v6, v5
	v_fmac_f32_e32 v6, v7, v4
	v_fma_f32 v2, -v2, v6, v5
	v_div_fmas_f32 v2, v2, v4, v6
	v_div_fixup_f32 v104, v2, v3, 1.0
	global_load_dwordx4 v[2:5], v[26:27], off
	global_load_dwordx4 v[6:9], v[62:63], off
	global_load_dwordx4 v[14:17], v[64:65], off
	v_pk_mul_f32 v[152:153], v[104:105], v[152:153] op_sel_hi:[0,1]
	v_pk_mul_f32 v[118:119], v[104:105], v[118:119] op_sel_hi:[0,1]
	s_waitcnt vmcnt(1)
	v_pk_add_f32 v[8:9], v[8:9], 1.0 op_sel_hi:[1,0]
	v_pk_add_f32 v[6:7], v[6:7], 1.0 op_sel_hi:[1,0]
	v_pk_mul_f32 v[160:161], v[4:5], v[8:9]
	v_pk_mul_f32 v[162:163], v[2:3], v[6:7]
	global_load_dwordx4 v[2:5], v[66:67], off
	global_load_dwordx4 v[10:13], v[68:69], off
	global_load_dwordx4 v[6:9], v[28:29], off
	s_waitcnt vmcnt(3)
	v_pk_fma_f32 v[156:157], v[162:163], v[156:157], v[14:15]
	v_pk_fma_f32 v[154:155], v[160:161], v[154:155], v[16:17]
	v_med3_f32 v47, v156, s33, v233
	v_med3_f32 v49, v157, s33, v233
	v_cvt_pk_fp8_f32 v51, v47, v49
	ds_read_b128 v[206:209], v105
	ds_read_b128 v[238:241], v105 offset:2048
	v_med3_f32 v47, v154, s33, v233
	v_med3_f32 v49, v155, s33, v233
	v_cvt_pk_fp8_f32 v51, v47, v49 op_sel:[0,0,1]
	v_pk_fma_f32 v[16:17], v[160:161], v[118:119], v[16:17]
	v_pk_fma_f32 v[14:15], v[162:163], v[152:153], v[14:15]
	v_add_co_u32_e32 v118, vcc, s80, v158
	s_waitcnt lgkmcnt(1)
	v_fma_f32 v224, v156, v206, 0
	v_addc_co_u32_e32 v119, vcc, 0, v159, vcc
	v_fma_f32 v223, v156, v207, 0
	v_fma_f32 v221, v156, v208, 0
	v_fma_f32 v217, v156, v209, 0
	v_fma_f32 v225, v14, v206, 0
	v_fma_f32 v222, v14, v207, 0
	v_fma_f32 v219, v14, v208, 0
	v_fma_f32 v215, v14, v209, 0
	ds_read_b128 v[206:209], v105 offset:1024
	global_store_dword v[118:119], v51, off
	v_med3_f32 v47, v14, s33, v233
	v_med3_f32 v49, v15, s33, v233
	v_mov_b32_e32 v51, 0
	v_cvt_pk_fp8_f32 v51, v47, v49
	v_med3_f32 v47, v16, s33, v233
	v_med3_f32 v49, v17, s33, v233
	s_waitcnt lgkmcnt(0)
	v_fma_f32 v220, v156, v206, 0
	v_fma_f32 v216, v156, v207, 0
	v_fma_f32 v213, v156, v208, 0
	v_fma_f32 v211, v156, v209, 0
	v_fma_f32 v218, v14, v206, 0
	v_fma_f32 v214, v14, v207, 0
	v_fma_f32 v212, v14, v208, 0
	v_fma_f32 v210, v14, v209, 0
	v_fma_f32 v209, v156, v238, 0
	v_fma_f32 v207, v156, v239, 0
	v_fma_f32 v205, v156, v240, 0
	v_fma_f32 v153, v156, v241, 0
	v_fma_f32 v208, v14, v238, 0
	v_fma_f32 v206, v14, v239, 0
	v_fma_f32 v158, v14, v240, 0
	v_fma_f32 v57, v14, v241, 0
	ds_read_b128 v[238:241], v105 offset:3072
	v_cvt_pk_fp8_f32 v51, v47, v49 op_sel:[0,0,1]
	global_store_dword v[118:119], v51, off offset:2048
	s_waitcnt lgkmcnt(0)
	v_fma_f32 v159, v156, v238, 0
	v_fma_f32 v152, v156, v239, 0
	v_fma_f32 v53, v156, v240, 0
	v_fma_f32 v49, v156, v241, 0
	v_fma_f32 v156, v14, v238, 0
	v_fma_f32 v55, v14, v239, 0
	v_fma_f32 v51, v14, v240, 0
	v_fma_f32 v47, v14, v241, 0
	ds_read_b128 v[238:241], v105 offset:4096
	s_waitcnt lgkmcnt(0)
	v_fmac_f32_e32 v224, v157, v238
	v_fmac_f32_e32 v223, v157, v239
	v_fmac_f32_e32 v221, v157, v240
	v_fmac_f32_e32 v217, v157, v241
	v_fmac_f32_e32 v225, v15, v238
	v_fmac_f32_e32 v222, v15, v239
	v_fmac_f32_e32 v219, v15, v240
	v_fmac_f32_e32 v215, v15, v241
	ds_read_b128 v[238:241], v105 offset:5120
	s_waitcnt lgkmcnt(0)
	v_fmac_f32_e32 v220, v157, v238
	v_fmac_f32_e32 v216, v157, v239
	v_fmac_f32_e32 v213, v157, v240
	v_fmac_f32_e32 v211, v157, v241
	v_fmac_f32_e32 v218, v15, v238
	v_fmac_f32_e32 v214, v15, v239
	v_fmac_f32_e32 v212, v15, v240
	v_fmac_f32_e32 v210, v15, v241
	ds_read_b128 v[238:241], v105 offset:6144
	s_waitcnt lgkmcnt(0)
	v_fmac_f32_e32 v209, v157, v238
	v_fmac_f32_e32 v207, v157, v239
	v_fmac_f32_e32 v205, v157, v240
	v_fmac_f32_e32 v153, v157, v241
	v_fmac_f32_e32 v208, v15, v238
	v_fmac_f32_e32 v206, v15, v239
	v_fmac_f32_e32 v158, v15, v240
	v_fmac_f32_e32 v57, v15, v241
	ds_read_b128 v[238:241], v105 offset:7168
	s_waitcnt lgkmcnt(0)
	v_fmac_f32_e32 v159, v157, v238
	v_fmac_f32_e32 v152, v157, v239
	v_fmac_f32_e32 v53, v157, v240
	v_fmac_f32_e32 v49, v157, v241
	v_fmac_f32_e32 v156, v15, v238
	v_fmac_f32_e32 v55, v15, v239
	v_fmac_f32_e32 v51, v15, v240
	v_fmac_f32_e32 v47, v15, v241
	ds_read_b128 v[238:241], v105 offset:8192
	s_waitcnt lgkmcnt(0)
	v_fmac_f32_e32 v224, v154, v238
	v_fmac_f32_e32 v223, v154, v239
	v_fmac_f32_e32 v221, v154, v240
	v_fmac_f32_e32 v217, v154, v241
	v_fmac_f32_e32 v225, v16, v238
	v_fmac_f32_e32 v222, v16, v239
	v_fmac_f32_e32 v219, v16, v240
	v_fmac_f32_e32 v215, v16, v241
	ds_read_b128 v[238:241], v105 offset:9216
	s_waitcnt lgkmcnt(0)
	v_fmac_f32_e32 v220, v154, v238
	v_fmac_f32_e32 v216, v154, v239
	v_fmac_f32_e32 v213, v154, v240
	v_fmac_f32_e32 v211, v154, v241
	v_fmac_f32_e32 v218, v16, v238
	v_fmac_f32_e32 v214, v16, v239
	v_fmac_f32_e32 v212, v16, v240
	v_fmac_f32_e32 v210, v16, v241
	ds_read_b128 v[238:241], v105 offset:10240
	s_waitcnt lgkmcnt(0)
	v_fmac_f32_e32 v209, v154, v238
	v_fmac_f32_e32 v207, v154, v239
	v_fmac_f32_e32 v205, v154, v240
	v_fmac_f32_e32 v153, v154, v241
	v_fmac_f32_e32 v208, v16, v238
	v_fmac_f32_e32 v206, v16, v239
	v_fmac_f32_e32 v158, v16, v240
	v_fmac_f32_e32 v57, v16, v241
	ds_read_b128 v[238:241], v105 offset:11264
	s_waitcnt lgkmcnt(0)
	v_fmac_f32_e32 v159, v154, v238
	v_fmac_f32_e32 v152, v154, v239
	v_fmac_f32_e32 v53, v154, v240
	v_fmac_f32_e32 v49, v154, v241
	v_fmac_f32_e32 v156, v16, v238
	v_fmac_f32_e32 v55, v16, v239
	v_fmac_f32_e32 v51, v16, v240
	v_fmac_f32_e32 v47, v16, v241
	ds_read_b128 v[238:241], v105 offset:12288
	s_waitcnt lgkmcnt(0)
	v_fmac_f32_e32 v224, v155, v238
	v_fmac_f32_e32 v223, v155, v239
	v_fmac_f32_e32 v221, v155, v240
	v_fmac_f32_e32 v217, v155, v241
	v_fmac_f32_e32 v225, v17, v238
	v_fmac_f32_e32 v222, v17, v239
	v_fmac_f32_e32 v219, v17, v240
	v_fmac_f32_e32 v215, v17, v241
	ds_read_b128 v[238:241], v105 offset:13312
	s_waitcnt lgkmcnt(0)
	v_fmac_f32_e32 v220, v155, v238
	v_fmac_f32_e32 v216, v155, v239
	v_fmac_f32_e32 v213, v155, v240
	v_fmac_f32_e32 v211, v155, v241
	v_fmac_f32_e32 v218, v17, v238
	v_fmac_f32_e32 v214, v17, v239
	v_fmac_f32_e32 v212, v17, v240
	v_fmac_f32_e32 v210, v17, v241
	ds_read_b128 v[238:241], v105 offset:14336
	s_waitcnt lgkmcnt(0)
	v_fmac_f32_e32 v209, v155, v238
	v_fmac_f32_e32 v207, v155, v239
	v_fmac_f32_e32 v205, v155, v240
	v_fmac_f32_e32 v153, v155, v241
	v_fmac_f32_e32 v208, v17, v238
	v_fmac_f32_e32 v206, v17, v239
	v_fmac_f32_e32 v158, v17, v240
	v_fmac_f32_e32 v57, v17, v241
	ds_read_b128 v[238:241], v105 offset:15360
	s_waitcnt lgkmcnt(0)
	v_fmac_f32_e32 v53, v155, v240
	v_fmac_f32_e32 v55, v17, v239
	v_fmac_f32_e32 v51, v17, v240
	v_fmac_f32_e32 v159, v155, v238
	v_fmac_f32_e32 v152, v155, v239
	v_fmac_f32_e32 v49, v155, v241
	v_fmac_f32_e32 v156, v17, v238
	v_fmac_f32_e32 v47, v17, v241
	s_waitcnt vmcnt(3)
	v_pk_add_f32 v[10:11], v[10:11], 1.0 op_sel_hi:[1,0]
	v_pk_mul_f32 v[150:151], v[102:103], v[150:151] op_sel_hi:[0,1]
	s_waitcnt vmcnt(2)
	v_pk_mul_f32 v[154:155], v[6:7], v[10:11]
	v_pk_add_f32 v[12:13], v[12:13], 1.0 op_sel_hi:[1,0]
	v_pk_fma_f32 v[160:161], v[150:151], v[154:155], v[2:3]
	v_pk_mul_f32 v[146:147], v[104:105], v[146:147] op_sel_hi:[0,1]
	v_pk_mul_f32 v[16:17], v[8:9], v[12:13]
	v_pk_mul_f32 v[14:15], v[102:103], v[148:149] op_sel_hi:[0,1]
	v_pk_mul_f32 v[144:145], v[104:105], v[144:145] op_sel_hi:[0,1]
	v_pk_fma_f32 v[154:155], v[154:155], v[146:147], v[2:3]
	v_med3_f32 v2, v160, s33, v233
	v_med3_f32 v3, v161, s33, v233
	v_mov_b32_e32 v148, 0
	v_pk_fma_f32 v[14:15], v[14:15], v[16:17], v[4:5]
	v_pk_fma_f32 v[16:17], v[16:17], v[144:145], v[4:5]
	v_cvt_pk_fp8_f32 v148, v2, v3
	v_med3_f32 v4, v154, s33, v233
	v_med3_f32 v5, v155, s33, v233
	v_mov_b32_e32 v149, 0
	v_cvt_pk_fp8_f32 v149, v4, v5
	v_med3_f32 v2, v14, s33, v233
	v_med3_f32 v3, v15, s33, v233
	v_cvt_pk_fp8_f32 v148, v2, v3 op_sel:[0,0,1]
	v_med3_f32 v2, v16, s33, v233
	v_med3_f32 v3, v17, s33, v233
	global_load_dwordx4 v[6:9], v[70:71], off
	global_load_dwordx4 v[10:13], v[72:73], off
	v_cvt_pk_fp8_f32 v149, v2, v3 op_sel:[0,0,1]
	global_load_dwordx4 v[2:5], v[30:31], off
	ds_read_b128 v[144:147], v105 offset:16384
	global_store_dword v[118:119], v148, off offset:256
	global_store_dword v[118:119], v149, off offset:2304
	ds_read_b128 v[148:151], v105 offset:17408
	s_waitcnt lgkmcnt(1)
	v_fmac_f32_e32 v224, v160, v144
	v_fmac_f32_e32 v223, v160, v145
	v_fmac_f32_e32 v221, v160, v146
	v_fmac_f32_e32 v217, v160, v147
	v_fmac_f32_e32 v225, v154, v144
	v_fmac_f32_e32 v222, v154, v145
	v_fmac_f32_e32 v219, v154, v146
	v_fmac_f32_e32 v215, v154, v147
	ds_read_b128 v[144:147], v105 offset:18432
	s_waitcnt lgkmcnt(1)
	v_fmac_f32_e32 v220, v160, v148
	v_fmac_f32_e32 v216, v160, v149
	v_fmac_f32_e32 v213, v160, v150
	v_fmac_f32_e32 v211, v160, v151
	v_fmac_f32_e32 v218, v154, v148
	v_fmac_f32_e32 v214, v154, v149
	v_fmac_f32_e32 v212, v154, v150
	v_fmac_f32_e32 v210, v154, v151
	ds_read_b128 v[148:151], v105 offset:19456
	s_waitcnt lgkmcnt(1)
	v_fmac_f32_e32 v209, v160, v144
	v_fmac_f32_e32 v207, v160, v145
	v_fmac_f32_e32 v205, v160, v146
	v_fmac_f32_e32 v153, v160, v147
	v_fmac_f32_e32 v208, v154, v144
	v_fmac_f32_e32 v206, v154, v145
	v_fmac_f32_e32 v158, v154, v146
	v_fmac_f32_e32 v57, v154, v147
	ds_read_b128 v[144:147], v105 offset:20480
	s_waitcnt lgkmcnt(1)
	v_fmac_f32_e32 v159, v160, v148
	v_fmac_f32_e32 v152, v160, v149
	v_fmac_f32_e32 v53, v160, v150
	v_fmac_f32_e32 v49, v160, v151
	v_fmac_f32_e32 v156, v154, v148
	v_fmac_f32_e32 v55, v154, v149
	v_fmac_f32_e32 v51, v154, v150
	v_fmac_f32_e32 v47, v154, v151
	ds_read_b128 v[148:151], v105 offset:21504
	s_waitcnt lgkmcnt(1)
	v_fmac_f32_e32 v224, v161, v144
	v_fmac_f32_e32 v223, v161, v145
	v_fmac_f32_e32 v221, v161, v146
	v_fmac_f32_e32 v217, v161, v147
	v_fmac_f32_e32 v225, v155, v144
	v_fmac_f32_e32 v222, v155, v145
	v_fmac_f32_e32 v219, v155, v146
	v_fmac_f32_e32 v215, v155, v147
	ds_read_b128 v[144:147], v105 offset:22528
	s_waitcnt lgkmcnt(1)
	v_fmac_f32_e32 v220, v161, v148
	v_fmac_f32_e32 v216, v161, v149
	v_fmac_f32_e32 v213, v161, v150
	v_fmac_f32_e32 v211, v161, v151
	v_fmac_f32_e32 v218, v155, v148
	v_fmac_f32_e32 v214, v155, v149
	v_fmac_f32_e32 v212, v155, v150
	v_fmac_f32_e32 v210, v155, v151
	ds_read_b128 v[148:151], v105 offset:23552
	s_waitcnt lgkmcnt(1)
	v_fmac_f32_e32 v209, v161, v144
	v_fmac_f32_e32 v207, v161, v145
	v_fmac_f32_e32 v205, v161, v146
	v_fmac_f32_e32 v153, v161, v147
	v_fmac_f32_e32 v208, v155, v144
	v_fmac_f32_e32 v206, v155, v145
	v_fmac_f32_e32 v158, v155, v146
	v_fmac_f32_e32 v57, v155, v147
	ds_read_b128 v[144:147], v105 offset:24576
	s_waitcnt lgkmcnt(1)
	v_fmac_f32_e32 v159, v161, v148
	v_fmac_f32_e32 v152, v161, v149
	v_fmac_f32_e32 v53, v161, v150
	v_fmac_f32_e32 v49, v161, v151
	v_fmac_f32_e32 v156, v155, v148
	v_fmac_f32_e32 v55, v155, v149
	v_fmac_f32_e32 v51, v155, v150
	v_fmac_f32_e32 v47, v155, v151
	ds_read_b128 v[148:151], v105 offset:25600
	s_waitcnt lgkmcnt(1)
	v_fmac_f32_e32 v224, v14, v144
	v_fmac_f32_e32 v223, v14, v145
	v_fmac_f32_e32 v221, v14, v146
	v_fmac_f32_e32 v217, v14, v147
	v_fmac_f32_e32 v225, v16, v144
	v_fmac_f32_e32 v222, v16, v145
	v_fmac_f32_e32 v219, v16, v146
	v_fmac_f32_e32 v215, v16, v147
	ds_read_b128 v[144:147], v105 offset:26624
	s_waitcnt lgkmcnt(1)
	v_fmac_f32_e32 v220, v14, v148
	v_fmac_f32_e32 v216, v14, v149
	v_fmac_f32_e32 v213, v14, v150
	v_fmac_f32_e32 v211, v14, v151
	v_fmac_f32_e32 v218, v16, v148
	v_fmac_f32_e32 v214, v16, v149
	v_fmac_f32_e32 v212, v16, v150
	v_fmac_f32_e32 v210, v16, v151
	ds_read_b128 v[148:151], v105 offset:27648
	s_waitcnt lgkmcnt(1)
	v_fmac_f32_e32 v209, v14, v144
	v_fmac_f32_e32 v207, v14, v145
	v_fmac_f32_e32 v205, v14, v146
	v_fmac_f32_e32 v153, v14, v147
	v_fmac_f32_e32 v208, v16, v144
	v_fmac_f32_e32 v206, v16, v145
	v_fmac_f32_e32 v158, v16, v146
	v_fmac_f32_e32 v57, v16, v147
	ds_read_b128 v[144:147], v105 offset:28672
	s_waitcnt lgkmcnt(1)
	v_fmac_f32_e32 v159, v14, v148
	v_fmac_f32_e32 v152, v14, v149
	v_fmac_f32_e32 v53, v14, v150
	v_fmac_f32_e32 v49, v14, v151
	v_fmac_f32_e32 v156, v16, v148
	v_fmac_f32_e32 v55, v16, v149
	v_fmac_f32_e32 v51, v16, v150
	v_fmac_f32_e32 v47, v16, v151
	ds_read_b128 v[148:151], v105 offset:29696
	s_waitcnt lgkmcnt(1)
	v_fmac_f32_e32 v224, v15, v144
	v_fmac_f32_e32 v223, v15, v145
	v_fmac_f32_e32 v221, v15, v146
	v_fmac_f32_e32 v217, v15, v147
	v_fmac_f32_e32 v225, v17, v144
	v_fmac_f32_e32 v222, v17, v145
	v_fmac_f32_e32 v219, v17, v146
	v_fmac_f32_e32 v215, v17, v147
	ds_read_b128 v[144:147], v105 offset:30720
	s_waitcnt lgkmcnt(1)
	v_fmac_f32_e32 v220, v15, v148
	v_fmac_f32_e32 v216, v15, v149
	v_fmac_f32_e32 v213, v15, v150
	v_fmac_f32_e32 v211, v15, v151
	v_fmac_f32_e32 v218, v17, v148
	v_fmac_f32_e32 v214, v17, v149
	v_fmac_f32_e32 v212, v17, v150
	v_fmac_f32_e32 v210, v17, v151
	ds_read_b128 v[148:151], v105 offset:31744
	s_waitcnt lgkmcnt(1)
	v_fmac_f32_e32 v57, v17, v147
	v_fmac_f32_e32 v209, v15, v144
	v_fmac_f32_e32 v207, v15, v145
	v_fmac_f32_e32 v205, v15, v146
	s_waitcnt lgkmcnt(0)
	v_fmac_f32_e32 v53, v15, v150
	v_fmac_f32_e32 v55, v17, v149
	v_fmac_f32_e32 v51, v17, v150
	v_fmac_f32_e32 v153, v15, v147
	v_fmac_f32_e32 v208, v17, v144
	v_fmac_f32_e32 v206, v17, v145
	v_fmac_f32_e32 v158, v17, v146
	v_fmac_f32_e32 v159, v15, v148
	v_fmac_f32_e32 v152, v15, v149
	v_fmac_f32_e32 v49, v15, v151
	v_fmac_f32_e32 v156, v17, v148
	v_fmac_f32_e32 v47, v17, v151
	s_waitcnt vmcnt(3)
	v_pk_add_f32 v[10:11], v[10:11], 1.0 op_sel_hi:[1,0]
	v_pk_mul_f32 v[142:143], v[102:103], v[142:143] op_sel_hi:[0,1]
	s_waitcnt vmcnt(2)
	v_pk_mul_f32 v[144:145], v[2:3], v[10:11]
	v_pk_add_f32 v[12:13], v[12:13], 1.0 op_sel_hi:[1,0]
	v_pk_fma_f32 v[146:147], v[142:143], v[144:145], v[6:7]
	v_pk_mul_f32 v[138:139], v[104:105], v[138:139] op_sel_hi:[0,1]
	v_pk_mul_f32 v[16:17], v[4:5], v[12:13]
	v_pk_mul_f32 v[14:15], v[102:103], v[140:141] op_sel_hi:[0,1]
	v_pk_mul_f32 v[136:137], v[104:105], v[136:137] op_sel_hi:[0,1]
	v_pk_fma_f32 v[144:145], v[138:139], v[144:145], v[6:7]
	v_med3_f32 v6, v146, s33, v233
	v_med3_f32 v7, v147, s33, v233
	v_mov_b32_e32 v140, 0
	v_pk_fma_f32 v[14:15], v[14:15], v[16:17], v[8:9]
	v_pk_fma_f32 v[16:17], v[136:137], v[16:17], v[8:9]
	v_cvt_pk_fp8_f32 v140, v6, v7
	v_med3_f32 v8, v144, s33, v233
	v_med3_f32 v9, v145, s33, v233
	v_mov_b32_e32 v141, 0
	v_cvt_pk_fp8_f32 v141, v8, v9
	v_med3_f32 v6, v14, s33, v233
	v_med3_f32 v7, v15, s33, v233
	v_cvt_pk_fp8_f32 v140, v6, v7 op_sel:[0,0,1]
	v_med3_f32 v6, v16, s33, v233
	v_med3_f32 v7, v17, s33, v233
	global_load_dwordx4 v[2:5], v[74:75], off
	global_load_dwordx4 v[10:13], v[76:77], off
	v_cvt_pk_fp8_f32 v141, v6, v7 op_sel:[0,0,1]
	global_load_dwordx4 v[6:9], v[32:33], off
	ds_read_b128 v[136:139], v105 offset:32768
	global_store_dword v[118:119], v140, off offset:512
	global_store_dword v[118:119], v141, off offset:2560
	ds_read_b128 v[140:143], v105 offset:33792
	s_waitcnt lgkmcnt(1)
	v_fmac_f32_e32 v224, v146, v136
	v_fmac_f32_e32 v223, v146, v137
	v_fmac_f32_e32 v221, v146, v138
	v_fmac_f32_e32 v217, v146, v139
	v_fmac_f32_e32 v225, v144, v136
	v_fmac_f32_e32 v222, v144, v137
	v_fmac_f32_e32 v219, v144, v138
	v_fmac_f32_e32 v215, v144, v139
	ds_read_b128 v[136:139], v105 offset:34816
	s_waitcnt lgkmcnt(1)
	v_fmac_f32_e32 v220, v146, v140
	v_fmac_f32_e32 v216, v146, v141
	v_fmac_f32_e32 v213, v146, v142
	v_fmac_f32_e32 v211, v146, v143
	v_fmac_f32_e32 v218, v144, v140
	v_fmac_f32_e32 v214, v144, v141
	v_fmac_f32_e32 v212, v144, v142
	v_fmac_f32_e32 v210, v144, v143
	ds_read_b128 v[140:143], v105 offset:35840
	s_waitcnt lgkmcnt(1)
	v_fmac_f32_e32 v209, v146, v136
	v_fmac_f32_e32 v207, v146, v137
	v_fmac_f32_e32 v205, v146, v138
	v_fmac_f32_e32 v153, v146, v139
	v_fmac_f32_e32 v208, v144, v136
	v_fmac_f32_e32 v206, v144, v137
	v_fmac_f32_e32 v158, v144, v138
	v_fmac_f32_e32 v57, v144, v139
	ds_read_b128 v[136:139], v105 offset:36864
	s_waitcnt lgkmcnt(1)
	v_fmac_f32_e32 v159, v146, v140
	v_fmac_f32_e32 v152, v146, v141
	v_fmac_f32_e32 v53, v146, v142
	v_fmac_f32_e32 v49, v146, v143
	v_fmac_f32_e32 v156, v144, v140
	v_fmac_f32_e32 v55, v144, v141
	v_fmac_f32_e32 v51, v144, v142
	v_fmac_f32_e32 v47, v144, v143
	ds_read_b128 v[140:143], v105 offset:37888
	s_waitcnt lgkmcnt(1)
	v_fmac_f32_e32 v224, v147, v136
	v_fmac_f32_e32 v223, v147, v137
	v_fmac_f32_e32 v221, v147, v138
	v_fmac_f32_e32 v217, v147, v139
	v_fmac_f32_e32 v225, v145, v136
	v_fmac_f32_e32 v222, v145, v137
	v_fmac_f32_e32 v219, v145, v138
	v_fmac_f32_e32 v215, v145, v139
	ds_read_b128 v[136:139], v105 offset:38912
	s_waitcnt lgkmcnt(1)
	v_fmac_f32_e32 v220, v147, v140
	v_fmac_f32_e32 v216, v147, v141
	v_fmac_f32_e32 v213, v147, v142
	v_fmac_f32_e32 v211, v147, v143
	v_fmac_f32_e32 v218, v145, v140
	v_fmac_f32_e32 v214, v145, v141
	v_fmac_f32_e32 v212, v145, v142
	v_fmac_f32_e32 v210, v145, v143
	ds_read_b128 v[140:143], v105 offset:39936
	s_waitcnt lgkmcnt(1)
	v_fmac_f32_e32 v209, v147, v136
	v_fmac_f32_e32 v207, v147, v137
	v_fmac_f32_e32 v205, v147, v138
	v_fmac_f32_e32 v153, v147, v139
	v_fmac_f32_e32 v208, v145, v136
	v_fmac_f32_e32 v206, v145, v137
	v_fmac_f32_e32 v158, v145, v138
	v_fmac_f32_e32 v57, v145, v139
	ds_read_b128 v[136:139], v105 offset:40960
	s_waitcnt lgkmcnt(1)
	v_fmac_f32_e32 v159, v147, v140
	v_fmac_f32_e32 v152, v147, v141
	v_fmac_f32_e32 v53, v147, v142
	v_fmac_f32_e32 v49, v147, v143
	v_fmac_f32_e32 v156, v145, v140
	v_fmac_f32_e32 v55, v145, v141
	v_fmac_f32_e32 v51, v145, v142
	v_fmac_f32_e32 v47, v145, v143
	ds_read_b128 v[140:143], v105 offset:41984
	s_waitcnt lgkmcnt(1)
	v_fmac_f32_e32 v224, v14, v136
	v_fmac_f32_e32 v223, v14, v137
	v_fmac_f32_e32 v221, v14, v138
	v_fmac_f32_e32 v217, v14, v139
	v_fmac_f32_e32 v225, v16, v136
	v_fmac_f32_e32 v222, v16, v137
	v_fmac_f32_e32 v219, v16, v138
	v_fmac_f32_e32 v215, v16, v139
	ds_read_b128 v[136:139], v105 offset:43008
	s_waitcnt lgkmcnt(1)
	v_fmac_f32_e32 v220, v14, v140
	v_fmac_f32_e32 v216, v14, v141
	v_fmac_f32_e32 v213, v14, v142
	v_fmac_f32_e32 v211, v14, v143
	v_fmac_f32_e32 v218, v16, v140
	v_fmac_f32_e32 v214, v16, v141
	v_fmac_f32_e32 v212, v16, v142
	v_fmac_f32_e32 v210, v16, v143
	ds_read_b128 v[140:143], v105 offset:44032
	s_waitcnt lgkmcnt(1)
	v_fmac_f32_e32 v209, v14, v136
	v_fmac_f32_e32 v207, v14, v137
	v_fmac_f32_e32 v205, v14, v138
	v_fmac_f32_e32 v153, v14, v139
	v_fmac_f32_e32 v208, v16, v136
	v_fmac_f32_e32 v206, v16, v137
	v_fmac_f32_e32 v158, v16, v138
	v_fmac_f32_e32 v57, v16, v139
	ds_read_b128 v[136:139], v105 offset:45056
	s_waitcnt lgkmcnt(1)
	v_fmac_f32_e32 v159, v14, v140
	v_fmac_f32_e32 v152, v14, v141
	v_fmac_f32_e32 v53, v14, v142
	v_fmac_f32_e32 v49, v14, v143
	v_fmac_f32_e32 v156, v16, v140
	v_fmac_f32_e32 v55, v16, v141
	v_fmac_f32_e32 v51, v16, v142
	v_fmac_f32_e32 v47, v16, v143
	ds_read_b128 v[140:143], v105 offset:46080
	s_waitcnt lgkmcnt(1)
	v_fmac_f32_e32 v224, v15, v136
	v_fmac_f32_e32 v223, v15, v137
	v_fmac_f32_e32 v221, v15, v138
	v_fmac_f32_e32 v217, v15, v139
	v_fmac_f32_e32 v225, v17, v136
	v_fmac_f32_e32 v222, v17, v137
	v_fmac_f32_e32 v219, v17, v138
	v_fmac_f32_e32 v215, v17, v139
	ds_read_b128 v[136:139], v105 offset:47104
	s_waitcnt lgkmcnt(1)
	v_fmac_f32_e32 v220, v15, v140
	v_fmac_f32_e32 v216, v15, v141
	v_fmac_f32_e32 v213, v15, v142
	v_fmac_f32_e32 v211, v15, v143
	v_fmac_f32_e32 v218, v17, v140
	v_fmac_f32_e32 v214, v17, v141
	v_fmac_f32_e32 v212, v17, v142
	v_fmac_f32_e32 v210, v17, v143
	ds_read_b128 v[140:143], v105 offset:48128
	s_waitcnt lgkmcnt(1)
	v_fmac_f32_e32 v57, v17, v139
	v_fmac_f32_e32 v209, v15, v136
	v_fmac_f32_e32 v207, v15, v137
	v_fmac_f32_e32 v205, v15, v138
	s_waitcnt lgkmcnt(0)
	v_fmac_f32_e32 v53, v15, v142
	v_fmac_f32_e32 v55, v17, v141
	v_fmac_f32_e32 v51, v17, v142
	v_fmac_f32_e32 v153, v15, v139
	v_fmac_f32_e32 v208, v17, v136
	v_fmac_f32_e32 v206, v17, v137
	v_fmac_f32_e32 v158, v17, v138
	v_fmac_f32_e32 v159, v15, v140
	v_fmac_f32_e32 v152, v15, v141
	v_fmac_f32_e32 v49, v15, v143
	v_fmac_f32_e32 v156, v17, v140
	v_fmac_f32_e32 v47, v17, v143
	s_waitcnt vmcnt(3)
	v_pk_add_f32 v[10:11], v[10:11], 1.0 op_sel_hi:[1,0]
	v_pk_mul_f32 v[130:131], v[102:103], v[130:131] op_sel_hi:[0,1]
	s_waitcnt vmcnt(2)
	v_pk_mul_f32 v[136:137], v[6:7], v[10:11]
	v_pk_add_f32 v[12:13], v[12:13], 1.0 op_sel_hi:[1,0]
	v_pk_mul_f32 v[14:15], v[102:103], v[128:129] op_sel_hi:[0,1]
	v_pk_fma_f32 v[138:139], v[130:131], v[136:137], v[2:3]
	v_pk_mul_f32 v[128:129], v[104:105], v[132:133] op_sel_hi:[0,1]
	v_pk_mul_f32 v[16:17], v[8:9], v[12:13]
	v_pk_mul_f32 v[130:131], v[104:105], v[134:135] op_sel_hi:[0,1]
	v_pk_fma_f32 v[136:137], v[128:129], v[136:137], v[2:3]
	v_med3_f32 v2, v138, s33, v233
	v_med3_f32 v3, v139, s33, v233
	v_mov_b32_e32 v132, 0
	v_pk_fma_f32 v[14:15], v[14:15], v[16:17], v[4:5]
	v_pk_fma_f32 v[16:17], v[130:131], v[16:17], v[4:5]
	v_cvt_pk_fp8_f32 v132, v2, v3
	v_med3_f32 v4, v136, s33, v233
	v_med3_f32 v5, v137, s33, v233
	v_mov_b32_e32 v133, 0
	v_cvt_pk_fp8_f32 v133, v4, v5
	v_med3_f32 v2, v14, s33, v233
	v_med3_f32 v3, v15, s33, v233
	v_cvt_pk_fp8_f32 v132, v2, v3 op_sel:[0,0,1]
	v_med3_f32 v2, v16, s33, v233
	v_med3_f32 v3, v17, s33, v233
	global_load_dwordx4 v[10:13], v[78:79], off
	global_load_dwordx4 v[6:9], v[80:81], off
	v_cvt_pk_fp8_f32 v133, v2, v3 op_sel:[0,0,1]
	global_load_dwordx4 v[2:5], v[34:35], off
	ds_read_b128 v[128:131], v105 offset:49152
	global_store_dword v[118:119], v132, off offset:768
	global_store_dword v[118:119], v133, off offset:2816
	ds_read_b128 v[132:135], v105 offset:50176
	s_waitcnt lgkmcnt(1)
	v_fmac_f32_e32 v224, v138, v128
	v_fmac_f32_e32 v223, v138, v129
	v_fmac_f32_e32 v221, v138, v130
	v_fmac_f32_e32 v217, v138, v131
	v_fmac_f32_e32 v225, v136, v128
	v_fmac_f32_e32 v222, v136, v129
	v_fmac_f32_e32 v219, v136, v130
	v_fmac_f32_e32 v215, v136, v131
	ds_read_b128 v[128:131], v105 offset:51200
	s_waitcnt lgkmcnt(1)
	v_fmac_f32_e32 v220, v138, v132
	v_fmac_f32_e32 v216, v138, v133
	v_fmac_f32_e32 v213, v138, v134
	v_fmac_f32_e32 v211, v138, v135
	v_fmac_f32_e32 v218, v136, v132
	v_fmac_f32_e32 v214, v136, v133
	v_fmac_f32_e32 v212, v136, v134
	v_fmac_f32_e32 v210, v136, v135
	ds_read_b128 v[132:135], v105 offset:52224
	s_waitcnt lgkmcnt(1)
	v_fmac_f32_e32 v209, v138, v128
	v_fmac_f32_e32 v207, v138, v129
	v_fmac_f32_e32 v205, v138, v130
	v_fmac_f32_e32 v153, v138, v131
	v_fmac_f32_e32 v208, v136, v128
	v_fmac_f32_e32 v206, v136, v129
	v_fmac_f32_e32 v158, v136, v130
	v_fmac_f32_e32 v57, v136, v131
	ds_read_b128 v[128:131], v105 offset:53248
	s_waitcnt lgkmcnt(1)
	v_fmac_f32_e32 v159, v138, v132
	v_fmac_f32_e32 v152, v138, v133
	v_fmac_f32_e32 v53, v138, v134
	v_fmac_f32_e32 v49, v138, v135
	v_fmac_f32_e32 v156, v136, v132
	v_fmac_f32_e32 v55, v136, v133
	v_fmac_f32_e32 v51, v136, v134
	v_fmac_f32_e32 v47, v136, v135
	ds_read_b128 v[132:135], v105 offset:54272
	s_waitcnt lgkmcnt(1)
	v_fmac_f32_e32 v224, v139, v128
	v_fmac_f32_e32 v223, v139, v129
	v_fmac_f32_e32 v221, v139, v130
	v_fmac_f32_e32 v217, v139, v131
	v_fmac_f32_e32 v225, v137, v128
	v_fmac_f32_e32 v222, v137, v129
	v_fmac_f32_e32 v219, v137, v130
	v_fmac_f32_e32 v215, v137, v131
	ds_read_b128 v[128:131], v105 offset:55296
	s_waitcnt lgkmcnt(1)
	v_fmac_f32_e32 v220, v139, v132
	v_fmac_f32_e32 v216, v139, v133
	v_fmac_f32_e32 v213, v139, v134
	v_fmac_f32_e32 v211, v139, v135
	v_fmac_f32_e32 v218, v137, v132
	v_fmac_f32_e32 v214, v137, v133
	v_fmac_f32_e32 v212, v137, v134
	v_fmac_f32_e32 v210, v137, v135
	ds_read_b128 v[132:135], v105 offset:56320
	s_waitcnt lgkmcnt(1)
	v_fmac_f32_e32 v209, v139, v128
	v_fmac_f32_e32 v207, v139, v129
	v_fmac_f32_e32 v205, v139, v130
	v_fmac_f32_e32 v153, v139, v131
	v_fmac_f32_e32 v208, v137, v128
	v_fmac_f32_e32 v206, v137, v129
	v_fmac_f32_e32 v158, v137, v130
	v_fmac_f32_e32 v57, v137, v131
	ds_read_b128 v[128:131], v105 offset:57344
	s_waitcnt lgkmcnt(1)
	v_fmac_f32_e32 v159, v139, v132
	v_fmac_f32_e32 v152, v139, v133
	v_fmac_f32_e32 v53, v139, v134
	v_fmac_f32_e32 v49, v139, v135
	v_fmac_f32_e32 v156, v137, v132
	v_fmac_f32_e32 v55, v137, v133
	v_fmac_f32_e32 v51, v137, v134
	v_fmac_f32_e32 v47, v137, v135
	ds_read_b128 v[132:135], v105 offset:58368
	s_waitcnt lgkmcnt(1)
	v_fmac_f32_e32 v224, v14, v128
	v_fmac_f32_e32 v223, v14, v129
	v_fmac_f32_e32 v221, v14, v130
	v_fmac_f32_e32 v217, v14, v131
	v_fmac_f32_e32 v225, v16, v128
	v_fmac_f32_e32 v222, v16, v129
	v_fmac_f32_e32 v219, v16, v130
	v_fmac_f32_e32 v215, v16, v131
	ds_read_b128 v[128:131], v105 offset:59392
	s_waitcnt lgkmcnt(1)
	v_fmac_f32_e32 v220, v14, v132
	v_fmac_f32_e32 v216, v14, v133
	v_fmac_f32_e32 v213, v14, v134
	v_fmac_f32_e32 v211, v14, v135
	v_fmac_f32_e32 v218, v16, v132
	v_fmac_f32_e32 v214, v16, v133
	v_fmac_f32_e32 v212, v16, v134
	v_fmac_f32_e32 v210, v16, v135
	ds_read_b128 v[132:135], v105 offset:60416
	s_waitcnt lgkmcnt(1)
	v_fmac_f32_e32 v209, v14, v128
	v_fmac_f32_e32 v207, v14, v129
	v_fmac_f32_e32 v205, v14, v130
	v_fmac_f32_e32 v153, v14, v131
	v_fmac_f32_e32 v208, v16, v128
	v_fmac_f32_e32 v206, v16, v129
	v_fmac_f32_e32 v158, v16, v130
	v_fmac_f32_e32 v57, v16, v131
	ds_read_b128 v[128:131], v105 offset:61440
	s_waitcnt lgkmcnt(1)
	v_fmac_f32_e32 v159, v14, v132
	v_fmac_f32_e32 v152, v14, v133
	v_fmac_f32_e32 v53, v14, v134
	v_fmac_f32_e32 v49, v14, v135
	v_fmac_f32_e32 v156, v16, v132
	v_fmac_f32_e32 v55, v16, v133
	v_fmac_f32_e32 v51, v16, v134
	v_fmac_f32_e32 v47, v16, v135
	ds_read_b128 v[132:135], v105 offset:62464
	s_waitcnt lgkmcnt(1)
	v_fmac_f32_e32 v224, v15, v128
	v_fmac_f32_e32 v223, v15, v129
	v_fmac_f32_e32 v221, v15, v130
	v_fmac_f32_e32 v217, v15, v131
	v_fmac_f32_e32 v225, v17, v128
	v_fmac_f32_e32 v222, v17, v129
	v_fmac_f32_e32 v219, v17, v130
	v_fmac_f32_e32 v215, v17, v131
	ds_read_b128 v[128:131], v105 offset:63488
	s_waitcnt lgkmcnt(1)
	v_fmac_f32_e32 v220, v15, v132
	v_fmac_f32_e32 v216, v15, v133
	v_fmac_f32_e32 v213, v15, v134
	v_fmac_f32_e32 v211, v15, v135
	v_fmac_f32_e32 v218, v17, v132
	v_fmac_f32_e32 v214, v17, v133
	v_fmac_f32_e32 v212, v17, v134
	v_fmac_f32_e32 v210, v17, v135
	ds_read_b128 v[132:135], v105 offset:64512
	s_waitcnt lgkmcnt(1)
	v_fmac_f32_e32 v57, v17, v131
	v_fmac_f32_e32 v209, v15, v128
	v_fmac_f32_e32 v207, v15, v129
	v_fmac_f32_e32 v205, v15, v130
	s_waitcnt lgkmcnt(0)
	v_fmac_f32_e32 v53, v15, v134
	v_fmac_f32_e32 v55, v17, v133
	v_fmac_f32_e32 v51, v17, v134
	v_fmac_f32_e32 v153, v15, v131
	v_fmac_f32_e32 v208, v17, v128
	v_fmac_f32_e32 v206, v17, v129
	v_fmac_f32_e32 v158, v17, v130
	v_fmac_f32_e32 v159, v15, v132
	v_fmac_f32_e32 v152, v15, v133
	v_fmac_f32_e32 v49, v15, v135
	v_fmac_f32_e32 v156, v17, v132
	v_fmac_f32_e32 v47, v17, v135
	s_waitcnt vmcnt(3)
	v_pk_add_f32 v[6:7], v[6:7], 1.0 op_sel_hi:[1,0]
	v_pk_mul_f32 v[126:127], v[102:103], v[126:127] op_sel_hi:[0,1]
	s_waitcnt vmcnt(2)
	v_pk_mul_f32 v[128:129], v[2:3], v[6:7]
	v_pk_add_f32 v[8:9], v[8:9], 1.0 op_sel_hi:[1,0]
	v_pk_fma_f32 v[130:131], v[126:127], v[128:129], v[10:11]
	v_pk_mul_f32 v[122:123], v[104:105], v[122:123] op_sel_hi:[0,1]
	v_pk_mul_f32 v[16:17], v[4:5], v[8:9]
	v_pk_mul_f32 v[14:15], v[102:103], v[124:125] op_sel_hi:[0,1]
	v_pk_mul_f32 v[120:121], v[104:105], v[120:121] op_sel_hi:[0,1]
	v_pk_fma_f32 v[128:129], v[122:123], v[128:129], v[10:11]
	v_med3_f32 v10, v130, s33, v233
	v_med3_f32 v11, v131, s33, v233
	v_mov_b32_e32 v124, 0
	v_pk_fma_f32 v[14:15], v[14:15], v[16:17], v[12:13]
	v_pk_fma_f32 v[16:17], v[120:121], v[16:17], v[12:13]
	v_cvt_pk_fp8_f32 v124, v10, v11
	v_med3_f32 v12, v128, s33, v233
	v_med3_f32 v13, v129, s33, v233
	v_mov_b32_e32 v125, 0
	v_cvt_pk_fp8_f32 v125, v12, v13
	v_med3_f32 v10, v14, s33, v233
	v_med3_f32 v11, v15, s33, v233
	v_cvt_pk_fp8_f32 v124, v10, v11 op_sel:[0,0,1]
	v_med3_f32 v10, v16, s33, v233
	v_med3_f32 v11, v17, s33, v233
	global_load_dwordx4 v[6:9], v[82:83], off
	global_load_dwordx4 v[2:5], v[84:85], off
	v_cvt_pk_fp8_f32 v125, v10, v11 op_sel:[0,0,1]
	v_add_u32_e32 v10, 0x10000, v105
	ds_read_b128 v[120:123], v10
	global_load_dwordx4 v[10:13], v[36:37], off
	s_nop 0
	global_store_dword v[118:119], v124, off offset:1024
	global_store_dword v[118:119], v125, off offset:3072
	v_add_u32_e32 v124, 0x10400, v105
	ds_read_b128 v[124:127], v124
	s_waitcnt lgkmcnt(1)
	v_fmac_f32_e32 v224, v130, v120
	v_fmac_f32_e32 v225, v128, v120
	v_add_u32_e32 v120, 0x10800, v105
	v_fmac_f32_e32 v223, v130, v121
	v_fmac_f32_e32 v221, v130, v122
	v_fmac_f32_e32 v217, v130, v123
	v_fmac_f32_e32 v222, v128, v121
	v_fmac_f32_e32 v219, v128, v122
	v_fmac_f32_e32 v215, v128, v123
	ds_read_b128 v[120:123], v120
	s_waitcnt lgkmcnt(1)
	v_fmac_f32_e32 v220, v130, v124
	v_fmac_f32_e32 v218, v128, v124
	v_add_u32_e32 v124, 0x10c00, v105
	v_fmac_f32_e32 v216, v130, v125
	v_fmac_f32_e32 v213, v130, v126
	v_fmac_f32_e32 v211, v130, v127
	v_fmac_f32_e32 v214, v128, v125
	v_fmac_f32_e32 v212, v128, v126
	v_fmac_f32_e32 v210, v128, v127
	ds_read_b128 v[124:127], v124
	s_waitcnt lgkmcnt(1)
	v_fmac_f32_e32 v209, v130, v120
	v_fmac_f32_e32 v208, v128, v120
	v_add_u32_e32 v120, 0x11000, v105
	v_fmac_f32_e32 v207, v130, v121
	v_fmac_f32_e32 v205, v130, v122
	v_fmac_f32_e32 v153, v130, v123
	v_fmac_f32_e32 v206, v128, v121
	v_fmac_f32_e32 v158, v128, v122
	v_fmac_f32_e32 v57, v128, v123
	ds_read_b128 v[120:123], v120
	s_waitcnt lgkmcnt(1)
	v_fmac_f32_e32 v159, v130, v124
	v_fmac_f32_e32 v156, v128, v124
	v_add_u32_e32 v124, 0x11400, v105
	v_fmac_f32_e32 v152, v130, v125
	v_fmac_f32_e32 v53, v130, v126
	v_fmac_f32_e32 v49, v130, v127
	v_fmac_f32_e32 v55, v128, v125
	v_fmac_f32_e32 v51, v128, v126
	v_fmac_f32_e32 v47, v128, v127
	ds_read_b128 v[124:127], v124
	s_waitcnt lgkmcnt(1)
	v_fmac_f32_e32 v224, v131, v120
	v_fmac_f32_e32 v225, v129, v120
	v_add_u32_e32 v120, 0x11800, v105
	v_fmac_f32_e32 v223, v131, v121
	v_fmac_f32_e32 v221, v131, v122
	v_fmac_f32_e32 v217, v131, v123
	v_fmac_f32_e32 v222, v129, v121
	v_fmac_f32_e32 v219, v129, v122
	v_fmac_f32_e32 v215, v129, v123
	ds_read_b128 v[120:123], v120
	s_waitcnt lgkmcnt(1)
	v_fmac_f32_e32 v220, v131, v124
	v_fmac_f32_e32 v218, v129, v124
	v_add_u32_e32 v124, 0x11c00, v105
	v_fmac_f32_e32 v216, v131, v125
	v_fmac_f32_e32 v213, v131, v126
	v_fmac_f32_e32 v211, v131, v127
	v_fmac_f32_e32 v214, v129, v125
	v_fmac_f32_e32 v212, v129, v126
	v_fmac_f32_e32 v210, v129, v127
	ds_read_b128 v[124:127], v124
	s_waitcnt lgkmcnt(1)
	v_fmac_f32_e32 v209, v131, v120
	v_fmac_f32_e32 v208, v129, v120
	v_add_u32_e32 v120, 0x12000, v105
	v_fmac_f32_e32 v207, v131, v121
	v_fmac_f32_e32 v205, v131, v122
	v_fmac_f32_e32 v153, v131, v123
	v_fmac_f32_e32 v206, v129, v121
	v_fmac_f32_e32 v158, v129, v122
	v_fmac_f32_e32 v57, v129, v123
	ds_read_b128 v[120:123], v120
	s_waitcnt lgkmcnt(1)
	v_fmac_f32_e32 v159, v131, v124
	v_fmac_f32_e32 v156, v129, v124
	v_add_u32_e32 v124, 0x12400, v105
	v_fmac_f32_e32 v152, v131, v125
	v_fmac_f32_e32 v53, v131, v126
	v_fmac_f32_e32 v49, v131, v127
	v_fmac_f32_e32 v55, v129, v125
	v_fmac_f32_e32 v51, v129, v126
	v_fmac_f32_e32 v47, v129, v127
	ds_read_b128 v[124:127], v124
	s_waitcnt lgkmcnt(1)
	v_fmac_f32_e32 v224, v14, v120
	v_fmac_f32_e32 v225, v16, v120
	v_add_u32_e32 v120, 0x12800, v105
	v_fmac_f32_e32 v223, v14, v121
	v_fmac_f32_e32 v221, v14, v122
	v_fmac_f32_e32 v217, v14, v123
	v_fmac_f32_e32 v222, v16, v121
	v_fmac_f32_e32 v219, v16, v122
	v_fmac_f32_e32 v215, v16, v123
	ds_read_b128 v[120:123], v120
	s_waitcnt lgkmcnt(1)
	v_fmac_f32_e32 v220, v14, v124
	v_fmac_f32_e32 v218, v16, v124
	v_add_u32_e32 v124, 0x12c00, v105
	v_fmac_f32_e32 v216, v14, v125
	v_fmac_f32_e32 v213, v14, v126
	v_fmac_f32_e32 v211, v14, v127
	v_fmac_f32_e32 v214, v16, v125
	v_fmac_f32_e32 v212, v16, v126
	v_fmac_f32_e32 v210, v16, v127
	ds_read_b128 v[124:127], v124
	s_waitcnt lgkmcnt(1)
	v_fmac_f32_e32 v209, v14, v120
	v_fmac_f32_e32 v207, v14, v121
	v_fmac_f32_e32 v205, v14, v122
	v_fmac_f32_e32 v153, v14, v123
	s_waitcnt lgkmcnt(0)
	v_fmac_f32_e32 v159, v14, v124
	v_fmac_f32_e32 v152, v14, v125
	v_fmac_f32_e32 v53, v14, v126
	v_fmac_f32_e32 v49, v14, v127
	v_add_u32_e32 v14, 0x13000, v105
	v_fmac_f32_e32 v208, v16, v120
	v_fmac_f32_e32 v206, v16, v121
	v_fmac_f32_e32 v158, v16, v122
	v_fmac_f32_e32 v57, v16, v123
	ds_read_b128 v[120:123], v14
	v_add_u32_e32 v14, 0x13400, v105
	v_fmac_f32_e32 v156, v16, v124
	v_fmac_f32_e32 v55, v16, v125
	v_fmac_f32_e32 v51, v16, v126
	v_fmac_f32_e32 v47, v16, v127
	ds_read_b128 v[124:127], v14
	v_add_u32_e32 v14, 0x13800, v105
	s_waitcnt lgkmcnt(1)
	v_fmac_f32_e32 v224, v15, v120
	v_fmac_f32_e32 v223, v15, v121
	v_fmac_f32_e32 v221, v15, v122
	v_fmac_f32_e32 v217, v15, v123
	v_fmac_f32_e32 v225, v17, v120
	v_fmac_f32_e32 v222, v17, v121
	v_fmac_f32_e32 v219, v17, v122
	v_fmac_f32_e32 v215, v17, v123
	ds_read_b128 v[120:123], v14
	v_add_u32_e32 v14, 0x13c00, v105
	s_waitcnt lgkmcnt(1)
	v_fmac_f32_e32 v220, v15, v124
	v_fmac_f32_e32 v216, v15, v125
	v_fmac_f32_e32 v213, v15, v126
	v_fmac_f32_e32 v211, v15, v127
	v_fmac_f32_e32 v218, v17, v124
	v_fmac_f32_e32 v214, v17, v125
	v_fmac_f32_e32 v212, v17, v126
	v_fmac_f32_e32 v210, v17, v127
	ds_read_b128 v[124:127], v14
	s_waitcnt lgkmcnt(1)
	v_fmac_f32_e32 v57, v17, v123
	v_fmac_f32_e32 v209, v15, v120
	v_fmac_f32_e32 v207, v15, v121
	v_fmac_f32_e32 v205, v15, v122
	s_waitcnt lgkmcnt(0)
	v_fmac_f32_e32 v53, v15, v126
	v_fmac_f32_e32 v55, v17, v125
	v_fmac_f32_e32 v51, v17, v126
	v_fmac_f32_e32 v153, v15, v123
	v_fmac_f32_e32 v208, v17, v120
	v_fmac_f32_e32 v206, v17, v121
	v_fmac_f32_e32 v158, v17, v122
	v_fmac_f32_e32 v159, v15, v124
	v_fmac_f32_e32 v152, v15, v125
	v_fmac_f32_e32 v49, v15, v127
	v_fmac_f32_e32 v156, v17, v124
	v_fmac_f32_e32 v47, v17, v127
	s_waitcnt vmcnt(3)
	v_pk_add_f32 v[2:3], v[2:3], 1.0 op_sel_hi:[1,0]
	v_pk_mul_f32 v[116:117], v[102:103], v[116:117] op_sel_hi:[0,1]
	s_waitcnt vmcnt(2)
	v_pk_mul_f32 v[120:121], v[10:11], v[2:3]
	v_pk_add_f32 v[4:5], v[4:5], 1.0 op_sel_hi:[1,0]
	v_pk_fma_f32 v[122:123], v[116:117], v[120:121], v[6:7]
	v_pk_mul_f32 v[112:113], v[104:105], v[112:113] op_sel_hi:[0,1]
	v_pk_mul_f32 v[16:17], v[12:13], v[4:5]
	v_pk_mul_f32 v[14:15], v[102:103], v[114:115] op_sel_hi:[0,1]
	v_pk_mul_f32 v[110:111], v[104:105], v[110:111] op_sel_hi:[0,1]
	v_pk_fma_f32 v[120:121], v[112:113], v[120:121], v[6:7]
	v_med3_f32 v6, v122, s33, v233
	v_med3_f32 v7, v123, s33, v233
	v_mov_b32_e32 v114, 0
	v_pk_fma_f32 v[14:15], v[14:15], v[16:17], v[8:9]
	v_pk_fma_f32 v[16:17], v[110:111], v[16:17], v[8:9]
	v_cvt_pk_fp8_f32 v114, v6, v7
	v_med3_f32 v8, v120, s33, v233
	v_med3_f32 v9, v121, s33, v233
	v_mov_b32_e32 v115, 0
	v_cvt_pk_fp8_f32 v115, v8, v9
	v_med3_f32 v6, v14, s33, v233
	v_med3_f32 v7, v15, s33, v233
	v_cvt_pk_fp8_f32 v114, v6, v7 op_sel:[0,0,1]
	v_med3_f32 v6, v16, s33, v233
	v_med3_f32 v7, v17, s33, v233
	v_cvt_pk_fp8_f32 v115, v6, v7 op_sel:[0,0,1]
	v_add_u32_e32 v6, 0x14000, v105
	global_load_dwordx4 v[2:5], v[86:87], off
	global_load_dwordx4 v[10:13], v[88:89], off
	ds_read_b128 v[110:113], v6
	global_load_dwordx4 v[6:9], v[38:39], off
	s_nop 0
	global_store_dword v[118:119], v114, off offset:1280
	global_store_dword v[118:119], v115, off offset:3328
	v_add_u32_e32 v114, 0x14400, v105
	ds_read_b128 v[114:117], v114
	s_waitcnt lgkmcnt(1)
	v_fmac_f32_e32 v224, v122, v110
	v_fmac_f32_e32 v225, v120, v110
	v_add_u32_e32 v110, 0x14800, v105
	v_fmac_f32_e32 v223, v122, v111
	v_fmac_f32_e32 v221, v122, v112
	v_fmac_f32_e32 v217, v122, v113
	v_fmac_f32_e32 v222, v120, v111
	v_fmac_f32_e32 v219, v120, v112
	v_fmac_f32_e32 v215, v120, v113
	ds_read_b128 v[110:113], v110
	s_waitcnt lgkmcnt(1)
	v_fmac_f32_e32 v220, v122, v114
	v_fmac_f32_e32 v218, v120, v114
	v_add_u32_e32 v114, 0x14c00, v105
	v_fmac_f32_e32 v216, v122, v115
	v_fmac_f32_e32 v213, v122, v116
	v_fmac_f32_e32 v211, v122, v117
	v_fmac_f32_e32 v214, v120, v115
	v_fmac_f32_e32 v212, v120, v116
	v_fmac_f32_e32 v210, v120, v117
	ds_read_b128 v[114:117], v114
	s_waitcnt lgkmcnt(1)
	v_fmac_f32_e32 v209, v122, v110
	v_fmac_f32_e32 v208, v120, v110
	v_add_u32_e32 v110, 0x15000, v105
	v_fmac_f32_e32 v207, v122, v111
	v_fmac_f32_e32 v205, v122, v112
	v_fmac_f32_e32 v153, v122, v113
	v_fmac_f32_e32 v206, v120, v111
	v_fmac_f32_e32 v158, v120, v112
	v_fmac_f32_e32 v57, v120, v113
	ds_read_b128 v[110:113], v110
	s_waitcnt lgkmcnt(1)
	v_fmac_f32_e32 v159, v122, v114
	v_fmac_f32_e32 v152, v122, v115
	v_fmac_f32_e32 v53, v122, v116
	v_fmac_f32_e32 v49, v122, v117
	v_fmac_f32_e32 v156, v120, v114
	v_fmac_f32_e32 v55, v120, v115
	v_fmac_f32_e32 v51, v120, v116
	v_fmac_f32_e32 v47, v120, v117
	ds_read_b128 v[114:117], v230
	s_waitcnt lgkmcnt(1)
	v_fmac_f32_e32 v224, v123, v110
	v_fmac_f32_e32 v223, v123, v111
	v_fmac_f32_e32 v221, v123, v112
	v_fmac_f32_e32 v217, v123, v113
	v_fmac_f32_e32 v225, v121, v110
	v_fmac_f32_e32 v222, v121, v111
	v_fmac_f32_e32 v219, v121, v112
	v_fmac_f32_e32 v215, v121, v113
	ds_read_b128 v[110:113], v250
	s_waitcnt lgkmcnt(1)
	v_fmac_f32_e32 v220, v123, v114
	v_fmac_f32_e32 v216, v123, v115
	v_fmac_f32_e32 v213, v123, v116
	v_fmac_f32_e32 v211, v123, v117
	v_fmac_f32_e32 v218, v121, v114
	v_fmac_f32_e32 v214, v121, v115
	v_fmac_f32_e32 v212, v121, v116
	v_fmac_f32_e32 v210, v121, v117
	ds_read_b128 v[114:117], v251
	s_waitcnt lgkmcnt(1)
	v_fmac_f32_e32 v209, v123, v110
	v_fmac_f32_e32 v207, v123, v111
	v_fmac_f32_e32 v205, v123, v112
	v_fmac_f32_e32 v153, v123, v113
	v_fmac_f32_e32 v208, v121, v110
	v_fmac_f32_e32 v206, v121, v111
	v_fmac_f32_e32 v158, v121, v112
	v_fmac_f32_e32 v57, v121, v113
	s_waitcnt lgkmcnt(0)
	v_fmac_f32_e32 v159, v123, v114
	v_fmac_f32_e32 v152, v123, v115
	v_fmac_f32_e32 v53, v123, v116
	v_fmac_f32_e32 v49, v123, v117
	v_fmac_f32_e32 v156, v121, v114
	ds_read_b128 v[110:113], v164
	v_fmac_f32_e32 v55, v121, v115
	v_fmac_f32_e32 v51, v121, v116
	v_fmac_f32_e32 v47, v121, v117
	ds_read_b128 v[114:117], v165
	s_waitcnt lgkmcnt(1)
	v_fmac_f32_e32 v224, v14, v110
	v_fmac_f32_e32 v223, v14, v111
	v_fmac_f32_e32 v221, v14, v112
	v_fmac_f32_e32 v217, v14, v113
	v_fmac_f32_e32 v225, v16, v110
	v_fmac_f32_e32 v222, v16, v111
	v_fmac_f32_e32 v219, v16, v112
	v_fmac_f32_e32 v215, v16, v113
	s_waitcnt lgkmcnt(0)
	v_fmac_f32_e32 v220, v14, v114
	v_fmac_f32_e32 v216, v14, v115
	v_fmac_f32_e32 v213, v14, v116
	v_fmac_f32_e32 v211, v14, v117
	v_fmac_f32_e32 v218, v16, v114
	ds_read_b128 v[110:113], v166
	v_fmac_f32_e32 v214, v16, v115
	v_fmac_f32_e32 v212, v16, v116
	v_fmac_f32_e32 v210, v16, v117
	ds_read_b128 v[114:117], v167
	s_waitcnt lgkmcnt(1)
	v_fmac_f32_e32 v209, v14, v110
	v_fmac_f32_e32 v207, v14, v111
	v_fmac_f32_e32 v205, v14, v112
	v_fmac_f32_e32 v153, v14, v113
	v_fmac_f32_e32 v208, v16, v110
	v_fmac_f32_e32 v206, v16, v111
	v_fmac_f32_e32 v158, v16, v112
	v_fmac_f32_e32 v57, v16, v113
	s_waitcnt lgkmcnt(0)
	v_fmac_f32_e32 v159, v14, v114
	v_fmac_f32_e32 v152, v14, v115
	v_fmac_f32_e32 v53, v14, v116
	v_fmac_f32_e32 v49, v14, v117
	v_fmac_f32_e32 v156, v16, v114
	ds_read_b128 v[110:113], v168
	v_fmac_f32_e32 v55, v16, v115
	v_fmac_f32_e32 v51, v16, v116
	v_fmac_f32_e32 v47, v16, v117
	ds_read_b128 v[114:117], v169
	s_waitcnt lgkmcnt(1)
	v_fmac_f32_e32 v224, v15, v110
	v_fmac_f32_e32 v223, v15, v111
	v_fmac_f32_e32 v221, v15, v112
	v_fmac_f32_e32 v217, v15, v113
	v_fmac_f32_e32 v225, v17, v110
	v_fmac_f32_e32 v222, v17, v111
	v_fmac_f32_e32 v219, v17, v112
	v_fmac_f32_e32 v215, v17, v113
	s_waitcnt lgkmcnt(0)
	v_fmac_f32_e32 v220, v15, v114
	v_fmac_f32_e32 v216, v15, v115
	v_fmac_f32_e32 v213, v15, v116
	v_fmac_f32_e32 v211, v15, v117
	v_fmac_f32_e32 v218, v17, v114
	ds_read_b128 v[110:113], v170
	v_fmac_f32_e32 v214, v17, v115
	v_fmac_f32_e32 v212, v17, v116
	v_fmac_f32_e32 v210, v17, v117
	ds_read_b128 v[114:117], v171
	s_waitcnt lgkmcnt(1)
	v_fmac_f32_e32 v57, v17, v113
	v_fmac_f32_e32 v209, v15, v110
	v_fmac_f32_e32 v207, v15, v111
	v_fmac_f32_e32 v205, v15, v112
	s_waitcnt lgkmcnt(0)
	v_fmac_f32_e32 v53, v15, v116
	v_fmac_f32_e32 v55, v17, v115
	v_fmac_f32_e32 v51, v17, v116
	v_fmac_f32_e32 v153, v15, v113
	v_fmac_f32_e32 v208, v17, v110
	v_fmac_f32_e32 v206, v17, v111
	v_fmac_f32_e32 v158, v17, v112
	v_fmac_f32_e32 v159, v15, v114
	v_fmac_f32_e32 v152, v15, v115
	v_fmac_f32_e32 v49, v15, v117
	v_fmac_f32_e32 v156, v17, v114
	v_fmac_f32_e32 v47, v17, v117
	s_waitcnt vmcnt(3)
	v_pk_add_f32 v[12:13], v[12:13], 1.0 op_sel_hi:[1,0]
	v_pk_add_f32 v[10:11], v[10:11], 1.0 op_sel_hi:[1,0]
	s_waitcnt vmcnt(2)
	v_pk_mul_f32 v[12:13], v[8:9], v[12:13]
	v_pk_mul_f32 v[10:11], v[6:7], v[10:11]
	global_load_dwordx4 v[6:9], v[90:91], off
	global_load_dwordx4 v[114:117], v[92:93], off
	global_load_dwordx4 v[120:123], v[40:41], off
	v_pk_mul_f32 v[14:15], v[102:103], v[108:109] op_sel_hi:[0,1]
	v_pk_mul_f32 v[16:17], v[102:103], v[106:107] op_sel_hi:[0,1]
	v_pk_fma_f32 v[106:107], v[16:17], v[12:13], v[4:5]
	v_pk_fma_f32 v[108:109], v[14:15], v[10:11], v[2:3]
	v_pk_mul_f32 v[14:15], v[104:105], v[20:21] op_sel_hi:[0,1]
	v_pk_mul_f32 v[16:17], v[104:105], v[18:19] op_sel_hi:[0,1]
	v_pk_fma_f32 v[110:111], v[16:17], v[12:13], v[4:5]
	v_pk_fma_f32 v[112:113], v[14:15], v[10:11], v[2:3]
	v_med3_f32 v2, v108, s33, v233
	v_med3_f32 v3, v109, s33, v233
	v_mov_b32_e32 v4, 0
	v_cvt_pk_fp8_f32 v4, v2, v3
	v_med3_f32 v2, v106, s33, v233
	v_med3_f32 v3, v107, s33, v233
	v_cvt_pk_fp8_f32 v4, v2, v3 op_sel:[0,0,1]
	v_med3_f32 v2, v112, s33, v233
	v_med3_f32 v3, v113, s33, v233
	global_store_dword v[118:119], v4, off offset:1536
	v_mov_b32_e32 v4, 0
	v_cvt_pk_fp8_f32 v4, v2, v3
	v_med3_f32 v2, v110, s33, v233
	v_med3_f32 v3, v111, s33, v233
	v_cvt_pk_fp8_f32 v4, v2, v3 op_sel:[0,0,1]
	global_store_dword v[118:119], v4, off offset:3584
	ds_read_b128 v[10:13], v172
	ds_read_b128 v[124:127], v173
	ds_read_b128 v[128:131], v174
	ds_read_b128 v[132:135], v175
	ds_read_b128 v[14:17], v176
	ds_read_b128 v[136:139], v177
	ds_read_b128 v[140:143], v178
	ds_read_b128 v[144:147], v179
	ds_read_b128 v[18:21], v180
	ds_read_b128 v[148:151], v181
	ds_read_b128 v[238:241], v182
	ds_read_b128 v[242:245], v183
	ds_read_b128 v[2:5], v184
	ds_read_b128 v[246:249], v185
	ds_read_b128 v[234:237], v186
	ds_read_b128 v[160:163], v187
	s_waitcnt vmcnt(3)
	v_pk_add_f32 v[116:117], v[116:117], 1.0 op_sel_hi:[1,0]
	v_pk_add_f32 v[154:155], v[114:115], 1.0 op_sel_hi:[1,0]
	s_waitcnt lgkmcnt(14)
	v_fmac_f32_e32 v215, v112, v13
	v_fmac_f32_e32 v219, v112, v12
	v_fmac_f32_e32 v222, v112, v11
	v_fmac_f32_e32 v225, v112, v10
	v_fmac_f32_e32 v217, v108, v13
	v_fmac_f32_e32 v221, v108, v12
	v_fmac_f32_e32 v223, v108, v11
	v_fmac_f32_e32 v224, v108, v10
	s_waitcnt vmcnt(2)
	v_pk_mul_f32 v[114:115], v[122:123], v[116:117]
	v_pk_mul_f32 v[116:117], v[120:121], v[154:155]
	s_waitcnt lgkmcnt(11)
	v_fmac_f32_e32 v215, v113, v17
	v_fmac_f32_e32 v219, v113, v16
	v_fmac_f32_e32 v222, v113, v15
	v_fmac_f32_e32 v225, v113, v14
	v_fmac_f32_e32 v217, v109, v17
	v_fmac_f32_e32 v221, v109, v16
	v_fmac_f32_e32 v223, v109, v15
	v_fmac_f32_e32 v224, v109, v14
	v_pk_mul_f32 v[10:11], v[102:103], v[100:101] op_sel_hi:[0,1]
	s_waitcnt lgkmcnt(7)
	v_fmac_f32_e32 v215, v110, v21
	v_fmac_f32_e32 v219, v110, v20
	v_fmac_f32_e32 v222, v110, v19
	v_fmac_f32_e32 v225, v110, v18
	v_fmac_f32_e32 v217, v106, v21
	v_fmac_f32_e32 v221, v106, v20
	v_fmac_f32_e32 v223, v106, v19
	v_fmac_f32_e32 v224, v106, v18
	v_pk_fma_f32 v[18:19], v[10:11], v[116:117], v[6:7]
	v_pk_mul_f32 v[10:11], v[104:105], v[96:97] op_sel_hi:[0,1]
	s_waitcnt lgkmcnt(3)
	v_fmac_f32_e32 v215, v111, v5
	v_fmac_f32_e32 v219, v111, v4
	v_fmac_f32_e32 v222, v111, v3
	v_fmac_f32_e32 v217, v107, v5
	v_fmac_f32_e32 v221, v107, v4
	v_fmac_f32_e32 v223, v107, v3
	v_pk_mul_f32 v[4:5], v[102:103], v[98:99] op_sel_hi:[0,1]
	v_pk_mul_f32 v[12:13], v[104:105], v[94:95] op_sel_hi:[0,1]
	v_pk_fma_f32 v[6:7], v[10:11], v[116:117], v[6:7]
	v_med3_f32 v3, v18, s33, v233
	v_med3_f32 v10, v19, s33, v233
	v_mov_b32_e32 v14, 0
	v_pk_fma_f32 v[4:5], v[4:5], v[114:115], v[8:9]
	v_pk_fma_f32 v[8:9], v[12:13], v[114:115], v[8:9]
	v_cvt_pk_fp8_f32 v14, v3, v10
	v_med3_f32 v11, v6, s33, v233
	v_med3_f32 v12, v7, s33, v233
	v_mov_b32_e32 v15, 0
	v_cvt_pk_fp8_f32 v15, v11, v12
	v_med3_f32 v3, v4, s33, v233
	v_med3_f32 v10, v5, s33, v233
	v_cvt_pk_fp8_f32 v14, v3, v10 op_sel:[0,0,1]
	v_med3_f32 v3, v8, s33, v233
	v_med3_f32 v10, v9, s33, v233
	v_cvt_pk_fp8_f32 v15, v3, v10 op_sel:[0,0,1]
	ds_read_b128 v[10:13], v188
	global_store_dword v[118:119], v14, off offset:1792
	global_store_dword v[118:119], v15, off offset:3840
	ds_read_b128 v[14:17], v189
	v_fmac_f32_e32 v210, v112, v127
	v_fmac_f32_e32 v212, v112, v126
	v_fmac_f32_e32 v214, v112, v125
	v_fmac_f32_e32 v218, v112, v124
	v_fmac_f32_e32 v211, v108, v127
	v_fmac_f32_e32 v213, v108, v126
	v_fmac_f32_e32 v216, v108, v125
	v_fmac_f32_e32 v220, v108, v124
	v_fmac_f32_e32 v210, v113, v139
	v_fmac_f32_e32 v212, v113, v138
	v_fmac_f32_e32 v214, v113, v137
	v_fmac_f32_e32 v218, v113, v136
	v_fmac_f32_e32 v211, v109, v139
	v_fmac_f32_e32 v213, v109, v138
	v_fmac_f32_e32 v216, v109, v137
	v_fmac_f32_e32 v220, v109, v136
	v_fmac_f32_e32 v210, v110, v151
	v_fmac_f32_e32 v212, v110, v150
	v_fmac_f32_e32 v214, v110, v149
	v_fmac_f32_e32 v218, v110, v148
	v_fmac_f32_e32 v211, v106, v151
	v_fmac_f32_e32 v213, v106, v150
	v_fmac_f32_e32 v216, v106, v149
	v_fmac_f32_e32 v220, v106, v148
	s_waitcnt lgkmcnt(4)
	v_fmac_f32_e32 v210, v111, v249
	v_fmac_f32_e32 v212, v111, v248
	v_fmac_f32_e32 v214, v111, v247
	v_fmac_f32_e32 v218, v111, v246
	v_fmac_f32_e32 v211, v107, v249
	v_fmac_f32_e32 v213, v107, v248
	v_fmac_f32_e32 v216, v107, v247
	v_fmac_f32_e32 v220, v107, v246
	v_fmac_f32_e32 v225, v111, v2
	v_fmac_f32_e32 v224, v107, v2
	s_waitcnt lgkmcnt(1)
	v_fmac_f32_e32 v224, v18, v10
	v_fmac_f32_e32 v223, v18, v11
	v_fmac_f32_e32 v221, v18, v12
	v_fmac_f32_e32 v217, v18, v13
	v_fmac_f32_e32 v225, v6, v10
	v_fmac_f32_e32 v222, v6, v11
	v_fmac_f32_e32 v219, v6, v12
	v_fmac_f32_e32 v215, v6, v13
	ds_read_b128 v[10:13], v190
	s_waitcnt lgkmcnt(1)
	v_fmac_f32_e32 v220, v18, v14
	v_fmac_f32_e32 v216, v18, v15
	v_fmac_f32_e32 v213, v18, v16
	v_fmac_f32_e32 v211, v18, v17
	v_fmac_f32_e32 v218, v6, v14
	v_fmac_f32_e32 v214, v6, v15
	v_fmac_f32_e32 v212, v6, v16
	v_fmac_f32_e32 v210, v6, v17
	ds_read_b128 v[14:17], v191
	v_fmac_f32_e32 v47, v112, v135
	v_fmac_f32_e32 v51, v112, v134
	v_fmac_f32_e32 v55, v112, v133
	v_fmac_f32_e32 v156, v112, v132
	v_fmac_f32_e32 v49, v108, v135
	v_fmac_f32_e32 v53, v108, v134
	v_fmac_f32_e32 v152, v108, v133
	v_fmac_f32_e32 v159, v108, v132
	v_fmac_f32_e32 v57, v112, v131
	v_fmac_f32_e32 v158, v112, v130
	v_fmac_f32_e32 v206, v112, v129
	v_fmac_f32_e32 v208, v112, v128
	v_fmac_f32_e32 v153, v108, v131
	v_fmac_f32_e32 v205, v108, v130
	v_fmac_f32_e32 v207, v108, v129
	v_fmac_f32_e32 v209, v108, v128
	v_fmac_f32_e32 v47, v113, v147
	v_fmac_f32_e32 v51, v113, v146
	v_fmac_f32_e32 v55, v113, v145
	v_fmac_f32_e32 v156, v113, v144
	v_fmac_f32_e32 v49, v109, v147
	v_fmac_f32_e32 v53, v109, v146
	v_fmac_f32_e32 v152, v109, v145
	v_fmac_f32_e32 v159, v109, v144
	v_fmac_f32_e32 v57, v113, v143
	v_fmac_f32_e32 v158, v113, v142
	v_fmac_f32_e32 v206, v113, v141
	v_fmac_f32_e32 v208, v113, v140
	v_fmac_f32_e32 v153, v109, v143
	v_fmac_f32_e32 v205, v109, v142
	v_fmac_f32_e32 v207, v109, v141
	v_fmac_f32_e32 v209, v109, v140
	v_fmac_f32_e32 v47, v110, v245
	v_fmac_f32_e32 v51, v110, v244
	v_fmac_f32_e32 v55, v110, v243
	v_fmac_f32_e32 v156, v110, v242
	v_fmac_f32_e32 v49, v106, v245
	v_fmac_f32_e32 v53, v106, v244
	v_fmac_f32_e32 v152, v106, v243
	v_fmac_f32_e32 v159, v106, v242
	v_fmac_f32_e32 v57, v110, v241
	v_fmac_f32_e32 v158, v110, v240
	v_fmac_f32_e32 v206, v110, v239
	v_fmac_f32_e32 v208, v110, v238
	v_fmac_f32_e32 v153, v106, v241
	v_fmac_f32_e32 v205, v106, v240
	v_fmac_f32_e32 v207, v106, v239
	v_fmac_f32_e32 v209, v106, v238
	v_fmac_f32_e32 v47, v111, v163
	v_fmac_f32_e32 v51, v111, v162
	v_fmac_f32_e32 v55, v111, v161
	v_fmac_f32_e32 v156, v111, v160
	v_fmac_f32_e32 v49, v107, v163
	v_fmac_f32_e32 v53, v107, v162
	v_fmac_f32_e32 v152, v107, v161
	v_fmac_f32_e32 v159, v107, v160
	v_fmac_f32_e32 v57, v111, v237
	v_fmac_f32_e32 v158, v111, v236
	v_fmac_f32_e32 v206, v111, v235
	v_fmac_f32_e32 v208, v111, v234
	v_fmac_f32_e32 v153, v107, v237
	v_fmac_f32_e32 v205, v107, v236
	v_fmac_f32_e32 v207, v107, v235
	v_fmac_f32_e32 v209, v107, v234
	s_waitcnt lgkmcnt(1)
	v_fmac_f32_e32 v209, v18, v10
	v_fmac_f32_e32 v207, v18, v11
	v_fmac_f32_e32 v205, v18, v12
	v_fmac_f32_e32 v153, v18, v13
	v_fmac_f32_e32 v208, v6, v10
	v_fmac_f32_e32 v206, v6, v11
	v_fmac_f32_e32 v158, v6, v12
	v_fmac_f32_e32 v57, v6, v13
	ds_read_b128 v[10:13], v192
	s_waitcnt lgkmcnt(1)
	v_fmac_f32_e32 v159, v18, v14
	v_fmac_f32_e32 v152, v18, v15
	v_fmac_f32_e32 v53, v18, v16
	v_fmac_f32_e32 v49, v18, v17
	v_fmac_f32_e32 v156, v6, v14
	v_fmac_f32_e32 v55, v6, v15
	v_fmac_f32_e32 v51, v6, v16
	v_fmac_f32_e32 v47, v6, v17
	ds_read_b128 v[14:17], v193
	s_waitcnt lgkmcnt(1)
	v_fmac_f32_e32 v224, v19, v10
	v_fmac_f32_e32 v223, v19, v11
	v_fmac_f32_e32 v221, v19, v12
	v_fmac_f32_e32 v217, v19, v13
	v_fmac_f32_e32 v225, v7, v10
	v_fmac_f32_e32 v222, v7, v11
	v_fmac_f32_e32 v219, v7, v12
	v_fmac_f32_e32 v215, v7, v13
	ds_read_b128 v[10:13], v194
	s_waitcnt lgkmcnt(1)
	v_fmac_f32_e32 v220, v19, v14
	v_fmac_f32_e32 v216, v19, v15
	v_fmac_f32_e32 v213, v19, v16
	v_fmac_f32_e32 v211, v19, v17
	v_fmac_f32_e32 v218, v7, v14
	v_fmac_f32_e32 v214, v7, v15
	v_fmac_f32_e32 v212, v7, v16
	v_fmac_f32_e32 v210, v7, v17
	ds_read_b128 v[14:17], v195
	s_waitcnt lgkmcnt(1)
	v_fmac_f32_e32 v209, v19, v10
	v_fmac_f32_e32 v207, v19, v11
	v_fmac_f32_e32 v205, v19, v12
	v_fmac_f32_e32 v153, v19, v13
	v_fmac_f32_e32 v208, v7, v10
	v_fmac_f32_e32 v206, v7, v11
	v_fmac_f32_e32 v158, v7, v12
	v_fmac_f32_e32 v57, v7, v13
	ds_read_b128 v[10:13], v196
	s_waitcnt lgkmcnt(1)
	v_fmac_f32_e32 v159, v19, v14
	v_fmac_f32_e32 v152, v19, v15
	v_fmac_f32_e32 v53, v19, v16
	v_fmac_f32_e32 v49, v19, v17
	v_fmac_f32_e32 v156, v7, v14
	v_fmac_f32_e32 v55, v7, v15
	v_fmac_f32_e32 v51, v7, v16
	v_fmac_f32_e32 v47, v7, v17
	ds_read_b128 v[14:17], v197
	s_waitcnt lgkmcnt(1)
	v_fmac_f32_e32 v224, v4, v10
	v_fmac_f32_e32 v223, v4, v11
	v_fmac_f32_e32 v221, v4, v12
	v_fmac_f32_e32 v217, v4, v13
	v_fmac_f32_e32 v225, v8, v10
	v_fmac_f32_e32 v222, v8, v11
	v_fmac_f32_e32 v219, v8, v12
	v_fmac_f32_e32 v215, v8, v13
	ds_read_b128 v[10:13], v198
	s_waitcnt lgkmcnt(1)
	v_fmac_f32_e32 v220, v4, v14
	v_fmac_f32_e32 v216, v4, v15
	v_fmac_f32_e32 v213, v4, v16
	v_fmac_f32_e32 v211, v4, v17
	v_fmac_f32_e32 v218, v8, v14
	v_fmac_f32_e32 v214, v8, v15
	v_fmac_f32_e32 v212, v8, v16
	v_fmac_f32_e32 v210, v8, v17
	ds_read_b128 v[14:17], v199
	s_waitcnt lgkmcnt(1)
	v_fmac_f32_e32 v209, v4, v10
	v_fmac_f32_e32 v207, v4, v11
	v_fmac_f32_e32 v205, v4, v12
	v_fmac_f32_e32 v153, v4, v13
	v_fmac_f32_e32 v208, v8, v10
	v_fmac_f32_e32 v206, v8, v11
	v_fmac_f32_e32 v158, v8, v12
	v_fmac_f32_e32 v57, v8, v13
	ds_read_b128 v[10:13], v200
	s_waitcnt lgkmcnt(1)
	v_fmac_f32_e32 v159, v4, v14
	v_fmac_f32_e32 v152, v4, v15
	v_fmac_f32_e32 v53, v4, v16
	v_fmac_f32_e32 v49, v4, v17
	v_fmac_f32_e32 v156, v8, v14
	v_fmac_f32_e32 v55, v8, v15
	v_fmac_f32_e32 v51, v8, v16
	v_fmac_f32_e32 v47, v8, v17
	ds_read_b128 v[14:17], v201
	s_waitcnt lgkmcnt(1)
	v_fmac_f32_e32 v224, v5, v10
	v_fmac_f32_e32 v223, v5, v11
	v_fmac_f32_e32 v221, v5, v12
	v_fmac_f32_e32 v217, v5, v13
	v_fmac_f32_e32 v225, v9, v10
	v_fmac_f32_e32 v222, v9, v11
	v_fmac_f32_e32 v219, v9, v12
	v_fmac_f32_e32 v215, v9, v13
	ds_read_b128 v[10:13], v202
	s_waitcnt lgkmcnt(1)
	v_fmac_f32_e32 v220, v5, v14
	v_fmac_f32_e32 v216, v5, v15
	v_fmac_f32_e32 v213, v5, v16
	v_fmac_f32_e32 v211, v5, v17
	v_fmac_f32_e32 v218, v9, v14
	v_fmac_f32_e32 v214, v9, v15
	v_fmac_f32_e32 v212, v9, v16
	v_fmac_f32_e32 v210, v9, v17
	ds_read_b128 v[14:17], v203
	s_waitcnt lgkmcnt(1)
	v_fmac_f32_e32 v57, v9, v13
	v_fmac_f32_e32 v209, v5, v10
	v_fmac_f32_e32 v207, v5, v11
	v_fmac_f32_e32 v205, v5, v12
	s_waitcnt lgkmcnt(0)
	v_fmac_f32_e32 v53, v5, v16
	v_fmac_f32_e32 v55, v9, v15
	v_fmac_f32_e32 v51, v9, v16
	v_fmac_f32_e32 v153, v5, v13
	v_fmac_f32_e32 v208, v9, v10
	v_fmac_f32_e32 v206, v9, v11
	v_fmac_f32_e32 v158, v9, v12
	v_fmac_f32_e32 v159, v5, v14
	v_fmac_f32_e32 v152, v5, v15
	v_fmac_f32_e32 v49, v5, v17
	v_fmac_f32_e32 v156, v9, v14
	v_fmac_f32_e32 v47, v9, v17
	ds_bpermute_b32 v10, v23, v221
	ds_bpermute_b32 v12, v23, v219
	ds_bpermute_b32 v14, v23, v217
	ds_bpermute_b32 v2, v23, v224
	ds_bpermute_b32 v3, v23, v225
	s_waitcnt lgkmcnt(4)
	v_add_f32_e32 v10, v221, v10
	ds_bpermute_b32 v11, v25, v10
	s_waitcnt lgkmcnt(4)
	v_add_f32_e32 v12, v219, v12
	ds_bpermute_b32 v13, v25, v12
	ds_bpermute_b32 v6, v23, v223
	ds_bpermute_b32 v8, v23, v222
	s_waitcnt lgkmcnt(3)
	v_add_f32_e32 v10, v10, v11
	ds_bpermute_b32 v11, v43, v10
	s_waitcnt lgkmcnt(3)
	v_add_f32_e32 v12, v12, v13
	ds_bpermute_b32 v13, v43, v12
	v_add_f32_e32 v2, v224, v2
	v_add_f32_e32 v3, v225, v3
	s_waitcnt lgkmcnt(1)
	v_add_f32_e32 v10, v10, v11
	ds_bpermute_b32 v11, v103, v10
	v_add_f32_e32 v6, v223, v6
	v_add_f32_e32 v8, v222, v8
	ds_bpermute_b32 v4, v25, v2
	ds_bpermute_b32 v5, v25, v3
	s_waitcnt lgkmcnt(2)
	v_add_f32_e32 v10, v10, v11
	v_mov_b32_e32 v11, v10
	s_nop 1
	v_permlane16_swap_b32_e32 v10, v11
	v_add_f32_e32 v19, v10, v11
	v_add_f32_e32 v10, v12, v13
	v_add_f32_e32 v12, v217, v14
	ds_bpermute_b32 v13, v25, v12
	ds_bpermute_b32 v11, v103, v10
	ds_bpermute_b32 v14, v23, v215
	ds_bpermute_b32 v7, v25, v6
	ds_bpermute_b32 v9, v25, v8
	s_waitcnt lgkmcnt(4)
	v_add_f32_e32 v12, v12, v13
	ds_bpermute_b32 v13, v43, v12
	s_waitcnt lgkmcnt(4)
	v_add_f32_e32 v10, v10, v11
	v_mov_b32_e32 v11, v10
	s_nop 1
	v_permlane16_swap_b32_e32 v10, v11
	v_add_f32_e32 v97, v10, v11
	s_waitcnt lgkmcnt(0)
	v_add_f32_e32 v10, v12, v13
	v_add_f32_e32 v12, v215, v14
	ds_bpermute_b32 v13, v25, v12
	ds_bpermute_b32 v11, v103, v10
	ds_bpermute_b32 v14, v23, v220
	v_add_f32_e32 v2, v2, v4
	v_add_f32_e32 v3, v3, v5
	s_waitcnt lgkmcnt(2)
	v_add_f32_e32 v12, v12, v13
	ds_bpermute_b32 v13, v43, v12
	s_waitcnt lgkmcnt(2)
	v_add_f32_e32 v10, v10, v11
	v_mov_b32_e32 v11, v10
	s_nop 1
	v_permlane16_swap_b32_e32 v10, v11
	v_add_f32_e32 v21, v10, v11
	s_waitcnt lgkmcnt(0)
	v_add_f32_e32 v10, v12, v13
	v_add_f32_e32 v12, v220, v14
	ds_bpermute_b32 v13, v25, v12
	ds_bpermute_b32 v11, v103, v10
	ds_bpermute_b32 v14, v23, v218
	v_add_f32_e32 v6, v6, v7
	v_add_f32_e32 v8, v8, v9
	s_waitcnt lgkmcnt(2)
	v_add_f32_e32 v12, v12, v13
	ds_bpermute_b32 v13, v43, v12
	s_waitcnt lgkmcnt(2)
	v_add_f32_e32 v10, v10, v11
	v_mov_b32_e32 v11, v10
	s_nop 1
	v_permlane16_swap_b32_e32 v10, v11
	v_add_f32_e32 v99, v10, v11
	s_waitcnt lgkmcnt(0)
	v_add_f32_e32 v10, v12, v13
	v_add_f32_e32 v12, v218, v14
	ds_bpermute_b32 v13, v25, v12
	ds_bpermute_b32 v11, v103, v10
	ds_bpermute_b32 v14, v23, v216
	ds_bpermute_b32 v4, v43, v2
	ds_bpermute_b32 v5, v43, v3
	s_waitcnt lgkmcnt(4)
	v_add_f32_e32 v12, v12, v13
	ds_bpermute_b32 v13, v43, v12
	s_waitcnt lgkmcnt(4)
	v_add_f32_e32 v10, v10, v11
	v_mov_b32_e32 v11, v10
	s_nop 1
	v_permlane16_swap_b32_e32 v10, v11
	v_add_f32_e32 v95, v10, v11
	s_waitcnt lgkmcnt(0)
	v_add_f32_e32 v10, v12, v13
	v_add_f32_e32 v12, v216, v14
	ds_bpermute_b32 v13, v25, v12
	ds_bpermute_b32 v11, v103, v10
	ds_bpermute_b32 v14, v23, v214
	ds_bpermute_b32 v7, v43, v6
	ds_bpermute_b32 v9, v43, v8
	s_waitcnt lgkmcnt(4)
	v_add_f32_e32 v12, v12, v13
	ds_bpermute_b32 v13, v43, v12
	s_waitcnt lgkmcnt(4)
	v_add_f32_e32 v10, v10, v11
	v_mov_b32_e32 v11, v10
	s_nop 1
	v_permlane16_swap_b32_e32 v10, v11
	v_add_f32_e32 v101, v10, v11
	s_waitcnt lgkmcnt(0)
	v_add_f32_e32 v10, v12, v13
	v_add_f32_e32 v12, v214, v14
	ds_bpermute_b32 v13, v25, v12
	ds_bpermute_b32 v11, v103, v10
	ds_bpermute_b32 v14, v23, v213
	v_add_f32_e32 v2, v2, v4
	v_add_f32_e32 v3, v3, v5
	s_waitcnt lgkmcnt(2)
	v_add_f32_e32 v12, v12, v13
	ds_bpermute_b32 v13, v43, v12
	s_waitcnt lgkmcnt(2)
	v_add_f32_e32 v10, v10, v11
	v_mov_b32_e32 v11, v10
	s_nop 1
	v_permlane16_swap_b32_e32 v10, v11
	v_add_f32_e32 v107, v10, v11
	s_waitcnt lgkmcnt(0)
	v_add_f32_e32 v10, v12, v13
	v_add_f32_e32 v12, v213, v14
	ds_bpermute_b32 v13, v25, v12
	ds_bpermute_b32 v11, v103, v10
	ds_bpermute_b32 v14, v23, v212
	v_add_f32_e32 v6, v6, v7
	v_add_f32_e32 v8, v8, v9
	s_waitcnt lgkmcnt(2)
	v_add_f32_e32 v12, v12, v13
	ds_bpermute_b32 v13, v43, v12
	s_waitcnt lgkmcnt(2)
	v_add_f32_e32 v10, v10, v11
	v_mov_b32_e32 v11, v10
	s_nop 1
	v_permlane16_swap_b32_e32 v10, v11
	v_add_f32_e32 v115, v10, v11
	s_waitcnt lgkmcnt(0)
	v_add_f32_e32 v10, v12, v13
	v_add_f32_e32 v12, v212, v14
	ds_bpermute_b32 v13, v25, v12
	ds_bpermute_b32 v11, v103, v10
	ds_bpermute_b32 v14, v23, v211
	ds_bpermute_b32 v4, v103, v2
	ds_bpermute_b32 v5, v103, v3
	s_waitcnt lgkmcnt(4)
	v_add_f32_e32 v12, v12, v13
	ds_bpermute_b32 v13, v43, v12
	s_waitcnt lgkmcnt(4)
	v_add_f32_e32 v10, v10, v11
	v_mov_b32_e32 v11, v10
	s_nop 1
	v_permlane16_swap_b32_e32 v10, v11
	v_add_f32_e32 v104, v10, v11
	s_waitcnt lgkmcnt(0)
	v_add_f32_e32 v10, v12, v13
	v_add_f32_e32 v12, v211, v14
	ds_bpermute_b32 v13, v25, v12
	ds_bpermute_b32 v11, v103, v10
	ds_bpermute_b32 v14, v23, v210
	ds_bpermute_b32 v7, v103, v6
	ds_bpermute_b32 v9, v103, v8
	s_waitcnt lgkmcnt(4)
	v_add_f32_e32 v12, v12, v13
	ds_bpermute_b32 v13, v43, v12
	s_waitcnt lgkmcnt(4)
	v_add_f32_e32 v10, v10, v11
	v_mov_b32_e32 v11, v10
	s_nop 1
	v_permlane16_swap_b32_e32 v10, v11
	v_add_f32_e32 v113, v10, v11
	s_waitcnt lgkmcnt(0)
	v_add_f32_e32 v10, v12, v13
	v_add_f32_e32 v12, v210, v14
	ds_bpermute_b32 v13, v25, v12
	ds_bpermute_b32 v11, v103, v10
	ds_bpermute_b32 v14, v23, v209
	v_add_f32_e32 v2, v2, v4
	v_add_f32_e32 v4, v3, v5
	s_waitcnt lgkmcnt(2)
	v_add_f32_e32 v12, v12, v13
	ds_bpermute_b32 v13, v43, v12
	s_waitcnt lgkmcnt(2)
	v_add_f32_e32 v10, v10, v11
	v_mov_b32_e32 v11, v10
	s_nop 1
	v_permlane16_swap_b32_e32 v10, v11
	v_add_f32_e32 v109, v10, v11
	s_waitcnt lgkmcnt(0)
	v_add_f32_e32 v10, v12, v13
	v_add_f32_e32 v12, v209, v14
	ds_bpermute_b32 v13, v25, v12
	ds_bpermute_b32 v11, v103, v10
	ds_bpermute_b32 v14, v23, v208
	v_add_f32_e32 v6, v6, v7
	v_add_f32_e32 v8, v8, v9
	s_waitcnt lgkmcnt(2)
	v_add_f32_e32 v12, v12, v13
	ds_bpermute_b32 v13, v43, v12
	s_waitcnt lgkmcnt(2)
	v_add_f32_e32 v10, v10, v11
	v_mov_b32_e32 v11, v10
	s_nop 1
	v_permlane16_swap_b32_e32 v10, v11
	v_add_f32_e32 v117, v10, v11
	s_waitcnt lgkmcnt(0)
	v_add_f32_e32 v10, v12, v13
	v_add_f32_e32 v12, v208, v14
	ds_bpermute_b32 v13, v25, v12
	ds_bpermute_b32 v11, v103, v10
	ds_bpermute_b32 v14, v23, v207
	v_mov_b32_e32 v3, v2
	v_mov_b32_e32 v5, v4
	s_waitcnt lgkmcnt(2)
	v_add_f32_e32 v12, v12, v13
	ds_bpermute_b32 v13, v43, v12
	s_waitcnt lgkmcnt(2)
	v_add_f32_e32 v10, v10, v11
	v_mov_b32_e32 v11, v10
	s_nop 1
	v_permlane16_swap_b32_e32 v10, v11
	v_add_f32_e32 v111, v10, v11
	s_waitcnt lgkmcnt(0)
	v_add_f32_e32 v10, v12, v13
	v_add_f32_e32 v12, v207, v14
	ds_bpermute_b32 v13, v25, v12
	ds_bpermute_b32 v11, v103, v10
	ds_bpermute_b32 v14, v23, v206
	v_mov_b32_e32 v7, v6
	v_mov_b32_e32 v9, v8
	s_waitcnt lgkmcnt(2)
	v_add_f32_e32 v12, v12, v13
	ds_bpermute_b32 v13, v43, v12
	s_waitcnt lgkmcnt(2)
	v_add_f32_e32 v10, v10, v11
	v_mov_b32_e32 v11, v10
	s_nop 1
	v_permlane16_swap_b32_e32 v10, v11
	v_add_f32_e32 v119, v10, v11
	s_waitcnt lgkmcnt(0)
	v_add_f32_e32 v10, v12, v13
	v_add_f32_e32 v12, v206, v14
	ds_bpermute_b32 v13, v25, v12
	ds_bpermute_b32 v11, v103, v10
	ds_bpermute_b32 v14, v23, v205
	v_permlane16_swap_b32_e32 v2, v3
	s_waitcnt lgkmcnt(2)
	v_add_f32_e32 v12, v12, v13
	ds_bpermute_b32 v13, v43, v12
	s_waitcnt lgkmcnt(2)
	v_add_f32_e32 v10, v10, v11
	v_mov_b32_e32 v11, v10
	s_nop 1
	v_permlane16_swap_b32_e32 v10, v11
	v_add_f32_e32 v123, v10, v11
	s_waitcnt lgkmcnt(0)
	v_add_f32_e32 v10, v12, v13
	v_add_f32_e32 v12, v205, v14
	ds_bpermute_b32 v13, v25, v12
	ds_bpermute_b32 v11, v103, v10
	ds_bpermute_b32 v14, v23, v158
	v_permlane16_swap_b32_e32 v4, v5
	s_waitcnt lgkmcnt(2)
	v_add_f32_e32 v12, v12, v13
	ds_bpermute_b32 v13, v43, v12
	s_waitcnt lgkmcnt(2)
	v_add_f32_e32 v10, v10, v11
	v_mov_b32_e32 v11, v10
	s_nop 1
	v_permlane16_swap_b32_e32 v10, v11
	v_add_f32_e32 v130, v10, v11
	s_waitcnt lgkmcnt(0)
	v_add_f32_e32 v10, v12, v13
	v_add_f32_e32 v12, v158, v14
	ds_bpermute_b32 v13, v25, v12
	ds_bpermute_b32 v11, v103, v10
	ds_bpermute_b32 v14, v23, v153
	v_permlane16_swap_b32_e32 v6, v7
	s_waitcnt lgkmcnt(2)
	v_add_f32_e32 v12, v12, v13
	ds_bpermute_b32 v13, v43, v12
	s_waitcnt lgkmcnt(2)
	v_add_f32_e32 v10, v10, v11
	v_mov_b32_e32 v11, v10
	s_nop 1
	v_permlane16_swap_b32_e32 v10, v11
	v_add_f32_e32 v121, v10, v11
	s_waitcnt lgkmcnt(0)
	v_add_f32_e32 v10, v12, v13
	v_add_f32_e32 v12, v153, v14
	ds_bpermute_b32 v13, v25, v12
	ds_bpermute_b32 v11, v103, v10
	ds_bpermute_b32 v14, v23, v57
	v_permlane16_swap_b32_e32 v8, v9
	s_waitcnt lgkmcnt(2)
	v_add_f32_e32 v12, v12, v13
	ds_bpermute_b32 v13, v43, v12
	s_waitcnt lgkmcnt(2)
	v_add_f32_e32 v10, v10, v11
	v_mov_b32_e32 v11, v10
	s_nop 1
	v_permlane16_swap_b32_e32 v10, v11
	v_add_f32_e32 v128, v10, v11
	s_waitcnt lgkmcnt(0)
	v_add_f32_e32 v10, v12, v13
	v_add_f32_e32 v12, v57, v14
	ds_bpermute_b32 v13, v25, v12
	ds_bpermute_b32 v11, v103, v10
	ds_bpermute_b32 v14, v23, v159
	v_add_f32_e32 v2, v2, v3
	v_add_f32_e32 v4, v4, v5
	s_waitcnt lgkmcnt(2)
	v_add_f32_e32 v12, v12, v13
	ds_bpermute_b32 v13, v43, v12
	s_waitcnt lgkmcnt(2)
	v_add_f32_e32 v10, v10, v11
	v_mov_b32_e32 v11, v10
	s_nop 1
	v_permlane16_swap_b32_e32 v10, v11
	v_add_f32_e32 v57, v10, v11
	s_waitcnt lgkmcnt(0)
	v_add_f32_e32 v10, v12, v13
	v_add_f32_e32 v12, v159, v14
	ds_bpermute_b32 v13, v25, v12
	ds_bpermute_b32 v11, v103, v10
	ds_bpermute_b32 v14, v23, v156
	v_add_f32_e32 v6, v6, v7
	v_add_f32_e32 v8, v8, v9
	s_waitcnt lgkmcnt(2)
	v_add_f32_e32 v12, v12, v13
	ds_bpermute_b32 v13, v43, v12
	s_waitcnt lgkmcnt(2)
	v_add_f32_e32 v10, v10, v11
	v_mov_b32_e32 v11, v10
	s_nop 1
	v_permlane16_swap_b32_e32 v10, v11
	v_add_f32_e32 v132, v10, v11
	s_waitcnt lgkmcnt(0)
	v_add_f32_e32 v10, v12, v13
	v_add_f32_e32 v12, v156, v14
	ds_bpermute_b32 v13, v25, v12
	ds_bpermute_b32 v11, v103, v10
	ds_bpermute_b32 v14, v23, v152
	v_mov_b32_e32 v3, v2
	v_mov_b32_e32 v5, v4
	s_waitcnt lgkmcnt(2)
	v_add_f32_e32 v12, v12, v13
	ds_bpermute_b32 v13, v43, v12
	s_waitcnt lgkmcnt(2)
	v_add_f32_e32 v10, v10, v11
	v_mov_b32_e32 v11, v10
	s_nop 1
	v_permlane16_swap_b32_e32 v10, v11
	v_add_f32_e32 v126, v10, v11
	s_waitcnt lgkmcnt(0)
	v_add_f32_e32 v10, v12, v13
	v_add_f32_e32 v12, v152, v14
	ds_bpermute_b32 v13, v25, v12
	ds_bpermute_b32 v11, v103, v10
	ds_bpermute_b32 v14, v23, v55
	v_mov_b32_e32 v7, v6
	v_mov_b32_e32 v9, v8
	s_waitcnt lgkmcnt(2)
	v_add_f32_e32 v12, v12, v13
	ds_bpermute_b32 v13, v43, v12
	s_waitcnt lgkmcnt(2)
	v_add_f32_e32 v10, v10, v11
	v_mov_b32_e32 v11, v10
	s_nop 1
	v_permlane16_swap_b32_e32 v10, v11
	v_add_f32_e32 v134, v10, v11
	s_waitcnt lgkmcnt(0)
	v_add_f32_e32 v10, v12, v13
	v_add_f32_e32 v12, v55, v14
	ds_bpermute_b32 v13, v25, v12
	ds_bpermute_b32 v11, v103, v10
	ds_bpermute_b32 v14, v23, v53
	v_mov_b32_e32 v20, v19
	v_mov_b32_e32 v98, v97
	s_waitcnt lgkmcnt(2)
	v_add_f32_e32 v12, v12, v13
	ds_bpermute_b32 v13, v43, v12
	s_waitcnt lgkmcnt(2)
	v_add_f32_e32 v10, v10, v11
	v_mov_b32_e32 v11, v10
	s_nop 1
	v_permlane16_swap_b32_e32 v10, v11
	v_add_f32_e32 v55, v10, v11
	s_waitcnt lgkmcnt(0)
	v_add_f32_e32 v10, v12, v13
	v_add_f32_e32 v12, v53, v14
	ds_bpermute_b32 v13, v25, v12
	ds_bpermute_b32 v11, v103, v10
	ds_bpermute_b32 v14, v23, v51
	v_mov_b32_e32 v94, v21
	v_mov_b32_e32 v100, v99
	s_waitcnt lgkmcnt(2)
	v_add_f32_e32 v12, v12, v13
	ds_bpermute_b32 v13, v43, v12
	s_waitcnt lgkmcnt(2)
	v_add_f32_e32 v10, v10, v11
	v_mov_b32_e32 v11, v10
	s_nop 1
	v_permlane16_swap_b32_e32 v10, v11
	v_add_f32_e32 v143, v10, v11
	s_waitcnt lgkmcnt(0)
	v_add_f32_e32 v10, v12, v13
	v_add_f32_e32 v12, v51, v14
	ds_bpermute_b32 v11, v103, v10
	ds_bpermute_b32 v13, v25, v12
	ds_bpermute_b32 v14, v23, v47
	v_mov_b32_e32 v96, v95
	v_mov_b32_e32 v102, v101
	s_waitcnt lgkmcnt(2)
	v_add_f32_e32 v10, v10, v11
	s_waitcnt lgkmcnt(1)
	v_add_f32_e32 v11, v12, v13
	ds_bpermute_b32 v12, v43, v11
	v_mov_b32_e32 v13, v10
	s_nop 1
	v_permlane16_swap_b32_e32 v10, v13
	v_add_f32_e32 v51, v10, v13
	s_waitcnt lgkmcnt(0)
	v_add_f32_e32 v10, v11, v12
	ds_bpermute_b32 v11, v103, v10
	ds_bpermute_b32 v12, v23, v49
	v_mov_b32_e32 v108, v107
	v_mov_b32_e32 v116, v115
	v_mov_b32_e32 v106, v104
	s_waitcnt lgkmcnt(1)
	v_add_f32_e32 v10, v10, v11
	s_waitcnt lgkmcnt(0)
	v_add_f32_e32 v11, v49, v12
	v_mov_b32_e32 v13, v10
	ds_bpermute_b32 v12, v25, v11
	s_nop 0
	v_permlane16_swap_b32_e32 v10, v13
	v_add_f32_e32 v141, v10, v13
	v_add_f32_e32 v10, v47, v14
	ds_bpermute_b32 v13, v25, v10
	s_waitcnt lgkmcnt(1)
	v_add_f32_e32 v11, v11, v12
	ds_bpermute_b32 v12, v43, v11
	v_mov_b32_e32 v114, v113
	v_mov_b32_e32 v110, v109
	s_waitcnt lgkmcnt(1)
	v_add_f32_e32 v10, v10, v13
	ds_bpermute_b32 v13, v43, v10
	s_waitcnt lgkmcnt(1)
	v_add_f32_e32 v11, v11, v12
	ds_bpermute_b32 v12, v103, v11
	v_mov_b32_e32 v118, v117
	v_mov_b32_e32 v112, v111
	s_waitcnt lgkmcnt(1)
	v_add_f32_e32 v10, v10, v13
	ds_bpermute_b32 v13, v103, v10
	s_waitcnt lgkmcnt(1)
	v_add_f32_e32 v11, v11, v12
	v_mov_b32_e32 v12, v11
	s_nop 1
	v_permlane16_swap_b32_e32 v11, v12
	s_waitcnt lgkmcnt(0)
	v_add_f32_e32 v10, v10, v13
	v_add_f32_e32 v136, v11, v12
	v_mov_b32_e32 v11, v10
	s_nop 1
	v_permlane16_swap_b32_e32 v10, v11
	v_add_f32_e32 v139, v10, v11
	v_mov_b32_e32 v120, v119
	v_mov_b32_e32 v124, v123
	v_mov_b32_e32 v131, v130
	v_mov_b32_e32 v122, v121
	v_mov_b32_e32 v129, v128
	v_mov_b32_e32 v125, v57
	v_mov_b32_e32 v133, v132
	v_mov_b32_e32 v127, v126
	v_mov_b32_e32 v135, v134
	v_mov_b32_e32 v137, v55
	v_mov_b32_e32 v144, v143
	v_mov_b32_e32 v53, v51
	v_mov_b32_e32 v142, v141
	v_mov_b32_e32 v138, v136
	v_mov_b32_e32 v140, v139
	v_permlane32_swap_b32_e32 v2, v3
	v_permlane32_swap_b32_e32 v4, v5
	v_permlane32_swap_b32_e32 v6, v7
	v_permlane32_swap_b32_e32 v8, v9
	v_permlane32_swap_b32_e32 v19, v20
	v_permlane32_swap_b32_e32 v97, v98
	v_permlane32_swap_b32_e32 v21, v94
	v_permlane32_swap_b32_e32 v99, v100
	v_permlane32_swap_b32_e32 v95, v96
	v_permlane32_swap_b32_e32 v101, v102
	v_permlane32_swap_b32_e32 v107, v108
	v_permlane32_swap_b32_e32 v115, v116
	v_permlane32_swap_b32_e32 v104, v106
	v_permlane32_swap_b32_e32 v113, v114
	v_permlane32_swap_b32_e32 v109, v110
	v_permlane32_swap_b32_e32 v117, v118
	v_permlane32_swap_b32_e32 v111, v112
	v_permlane32_swap_b32_e32 v119, v120
	v_permlane32_swap_b32_e32 v123, v124
	v_permlane32_swap_b32_e32 v130, v131
	v_permlane32_swap_b32_e32 v121, v122
	v_permlane32_swap_b32_e32 v128, v129
	v_permlane32_swap_b32_e32 v57, v125
	v_permlane32_swap_b32_e32 v132, v133
	v_permlane32_swap_b32_e32 v126, v127
	v_permlane32_swap_b32_e32 v134, v135
	v_permlane32_swap_b32_e32 v55, v137
	v_permlane32_swap_b32_e32 v143, v144
	v_permlane32_swap_b32_e32 v51, v53
	v_permlane32_swap_b32_e32 v141, v142
	v_permlane32_swap_b32_e32 v136, v138
	v_permlane32_swap_b32_e32 v139, v140
	s_and_saveexec_b64 s[4:5], s[42:43]
	s_cbranch_execz .LBB0_1299
	v_add_f32_e32 v4, v4, v5
	v_add_f32_e32 v2, v2, v3
	v_cndmask_b32_e64 v2, v2, v4, s[40:41]
	v_mul_f32_e32 v2, 0xbfb8aa3b, v2
	s_load_dwordx2 s[6:7], s[56:57], 0xd0
	v_exp_f32_e32 v2, v2
	v_add_f32_e32 v8, v8, v9
	v_add_f32_e32 v6, v6, v7
	v_cndmask_b32_e64 v49, v6, v8, s[40:41]
	v_add_f32_e32 v2, 1.0, v2
	v_rcp_f32_e32 v18, v2
	s_waitcnt lgkmcnt(0)
	global_load_dwordx4 v[2:5], v1, s[6:7] offset:48
	global_load_dwordx4 v[6:9], v1, s[6:7] offset:32
	global_load_dwordx4 v[10:13], v1, s[6:7] offset:16
	global_load_dwordx4 v[14:17], v1, s[6:7]
	s_mov_b32 s6, 0xf149f2ca
	s_waitcnt vmcnt(0)
	v_add_f32_e32 v47, v18, v14
	v_mul_f32_e32 v14, 0xbfb8aa3b, v49
	v_exp_f32_e32 v14, v14
	v_cmp_nlt_f32_e32 vcc, s6, v47
	v_add_f32_e32 v14, 1.0, v14
	v_rcp_f32_e32 v14, v14
	s_nop 0
	v_add_f32_e32 v49, v14, v15
	v_mov_b32_e32 v15, 0xf149f2ca
	v_cndmask_b32_e32 v145, v47, v15, vcc
	v_cmp_gt_f32_e64 s[44:45], v49, v145
	v_cmp_ngt_f32_e64 s[46:47], v49, v145
	v_mov_b32_e32 v148, v49
	v_mov_b32_e32 v147, v145
	s_and_saveexec_b64 s[6:7], s[46:47]
	s_cbranch_execz .LBB0_1305
	v_mov_b32_e32 v147, 0xf149f2ca
	v_cmp_gt_f32_e64 s[46:47], v49, v147
	s_and_saveexec_b64 s[8:9], s[46:47]
	v_mov_b32_e32 v147, v49
	s_or_b64 exec, exec, s[8:9]
	v_mov_b32_e32 v148, v145
